# speedup vs baseline: 1.0125x; 1.0037x over previous
.LBB1_23:
	s_or_b64 exec, exec, s[26:27]
	s_lshr_b32 s0, s24, 7
	s_and_b32 s21, s0, 14
	s_and_b32 s0, s33, -8
	v_or_b32_e32 v217, v205, v204
	v_bfe_u32 v216, v0, 4, 2
	s_cmp_lg_u32 s0, 16
	s_mov_b64 s[0:1], -1
	s_cbranch_scc0 .LBB1_57
	v_lshlrev_b32_e32 v130, 2, v216
	s_and_b32 s23, s20, 0x700
	v_lshl_or_b32 v206, v214, 5, v130
	v_or_b32_e32 v130, s23, v217
	v_lshrrev_b32_e32 v131, 1, v206
	v_lshlrev_b32_e32 v130, 6, v130
	v_or_b32_e32 v132, v130, v131
	v_lshlrev_b32_e32 v132, 4, v132
	global_load_dwordx4 v[186:189], v132, s[16:17] offset:16
	global_load_dwordx4 v[190:193], v132, s[16:17]
	v_or_b32_e32 v132, 8, v131
	v_or_b32_e32 v133, v130, v132
	v_lshlrev_b32_e32 v133, 4, v133
	global_load_dwordx4 v[178:181], v133, s[16:17] offset:16
	global_load_dwordx4 v[182:185], v133, s[16:17]
	v_or_b32_e32 v133, 0x400, v130
	v_or_b32_e32 v134, v133, v131
	v_or_b32_e32 v133, v133, v132
	v_lshlrev_b32_e32 v134, 4, v134
	v_lshlrev_b32_e32 v133, 4, v133
	global_load_dwordx4 v[170:173], v134, s[16:17] offset:16
	global_load_dwordx4 v[174:177], v134, s[16:17]
	global_load_dwordx4 v[162:165], v133, s[16:17] offset:16
	global_load_dwordx4 v[166:169], v133, s[16:17]
	v_or_b32_e32 v133, 0x800, v130
	s_cmp_lt_u32 s33, 8
	v_or_b32_e32 v134, v133, v131
	v_or_b32_e32 v130, 0xc00, v130
	s_cselect_b64 vcc, -1, 0
	v_lshlrev_b32_e32 v134, 4, v134
	v_or_b32_e32 v133, v133, v132
	v_or_b32_e32 v131, v130, v131
	v_or_b32_e32 v130, v130, v132
	s_and_b64 s[0:1], vcc, exec
	global_load_dwordx4 v[154:157], v134, s[16:17] offset:16
	global_load_dwordx4 v[158:161], v134, s[16:17]
	v_lshlrev_b32_e32 v133, 4, v133
	v_lshlrev_b32_e32 v131, 4, v131
	v_lshlrev_b32_e32 v134, 4, v130
	s_cselect_b32 s1, s19, s5
	s_cselect_b32 s0, s18, s4
	v_lshlrev_b32_e32 v194, 2, v206
	global_load_dwordx4 v[146:149], v133, s[16:17] offset:16
	global_load_dwordx4 v[150:153], v133, s[16:17]
	global_load_dwordx4 v[138:141], v131, s[16:17] offset:16
	global_load_dwordx4 v[142:145], v131, s[16:17]
	s_nop 0
	global_load_dwordx4 v[130:133], v134, s[16:17] offset:16
	s_nop 0
	global_load_dwordx4 v[134:137], v134, s[16:17]
	s_nop 0
	global_load_dwordx4 v[198:201], v194, s[0:1]
	s_nop 0
	global_load_dwordx4 v[194:197], v194, s[0:1] offset:64
	v_fma_f32 v218, v122, v122, 0
	v_fmac_f32_e32 v218, v123, v123
	v_fmac_f32_e32 v218, v124, v124
	v_fmac_f32_e32 v218, v125, v125
	v_fmac_f32_e32 v218, v114, v114
	v_fmac_f32_e32 v218, v115, v115
	v_fmac_f32_e32 v218, v116, v116
	v_fmac_f32_e32 v218, v117, v117
	v_mov_b32_e32 v219, v218
	s_nop 1
	v_permlane16_swap_b32_e32 v218, v219
	s_add_i32 s24, 0, 0x21000
	v_add_f32_e32 v219, v218, v219
	v_lshl_add_u32 v207, v214, 2, s24
	v_mov_b32_e32 v220, v219
	v_cmp_eq_u32_e64 s[0:1], 0, v216
	s_nop 0
	v_permlane32_swap_b32_e32 v219, v220
	v_lshl_add_u32 v218, v217, 4, v207
	s_barrier
	s_and_saveexec_b64 s[24:25], s[0:1]
	v_add_f32_e32 v219, v219, v220
	ds_write_b32 v218, v219
	s_or_b64 exec, exec, s[24:25]
	v_fma_f32 v219, v102, v102, 0
	v_fmac_f32_e32 v219, v103, v103
	v_fmac_f32_e32 v219, v104, v104
	v_fmac_f32_e32 v219, v105, v105
	v_fmac_f32_e32 v219, v98, v98
	v_fmac_f32_e32 v219, v99, v99
	v_fmac_f32_e32 v219, v100, v100
	v_fmac_f32_e32 v219, v101, v101
	v_mov_b32_e32 v220, v219
	s_nop 1
	v_permlane16_swap_b32_e32 v219, v220
	v_add_f32_e32 v219, v219, v220
	v_mov_b32_e32 v220, v219
	s_nop 1
	v_permlane32_swap_b32_e32 v219, v220
	s_and_saveexec_b64 s[24:25], s[0:1]
	v_add_f32_e32 v219, v219, v220
	ds_write_b32 v218, v219 offset:256
	s_or_b64 exec, exec, s[24:25]
	v_fma_f32 v219, v86, v86, 0
	v_fmac_f32_e32 v219, v87, v87
	v_fmac_f32_e32 v219, v88, v88
	v_fmac_f32_e32 v219, v89, v89
	v_fmac_f32_e32 v219, v82, v82
	v_fmac_f32_e32 v219, v83, v83
	v_fmac_f32_e32 v219, v84, v84
	v_fmac_f32_e32 v219, v85, v85
	v_mov_b32_e32 v220, v219
	s_nop 1
	v_permlane16_swap_b32_e32 v219, v220
	v_add_f32_e32 v219, v219, v220
	v_mov_b32_e32 v220, v219
	s_nop 1
	v_permlane32_swap_b32_e32 v219, v220
	s_and_saveexec_b64 s[24:25], s[0:1]
	v_add_f32_e32 v219, v219, v220
	ds_write_b32 v218, v219 offset:512
	s_or_b64 exec, exec, s[24:25]
	v_fma_f32 v219, v70, v70, 0
	v_fmac_f32_e32 v219, v71, v71
	v_fmac_f32_e32 v219, v72, v72
	v_fmac_f32_e32 v219, v73, v73
	v_fmac_f32_e32 v219, v58, v58
	v_fmac_f32_e32 v219, v59, v59
	v_fmac_f32_e32 v219, v60, v60
	v_fmac_f32_e32 v219, v61, v61
	v_mov_b32_e32 v220, v219
	s_nop 1
	v_permlane16_swap_b32_e32 v219, v220
	v_add_f32_e32 v219, v219, v220
	v_mov_b32_e32 v220, v219
	s_nop 1
	v_permlane32_swap_b32_e32 v219, v220
	s_and_saveexec_b64 s[24:25], s[0:1]
	v_add_f32_e32 v219, v219, v220
	ds_write_b32 v218, v219 offset:768
	s_or_b64 exec, exec, s[24:25]
	v_fma_f32 v219, v66, v66, 0
	v_fmac_f32_e32 v219, v67, v67
	v_fmac_f32_e32 v219, v68, v68
	v_fmac_f32_e32 v219, v69, v69
	v_fmac_f32_e32 v219, v50, v50
	v_fmac_f32_e32 v219, v51, v51
	v_fmac_f32_e32 v219, v52, v52
	v_fmac_f32_e32 v219, v53, v53
	v_mov_b32_e32 v220, v219
	s_nop 1
	v_permlane16_swap_b32_e32 v219, v220
	v_add_f32_e32 v219, v219, v220
	v_mov_b32_e32 v220, v219
	s_nop 1
	v_permlane32_swap_b32_e32 v219, v220
	s_and_saveexec_b64 s[24:25], s[0:1]
	v_add_f32_e32 v219, v219, v220
	ds_write_b32 v218, v219 offset:2048
	s_or_b64 exec, exec, s[24:25]
	v_fma_f32 v219, v46, v46, 0
	v_fmac_f32_e32 v219, v47, v47
	v_fmac_f32_e32 v219, v48, v48
	v_fmac_f32_e32 v219, v49, v49
	v_fmac_f32_e32 v219, v34, v34
	v_fmac_f32_e32 v219, v35, v35
	v_fmac_f32_e32 v219, v36, v36
	v_fmac_f32_e32 v219, v37, v37
	v_mov_b32_e32 v220, v219
	s_nop 1
	v_permlane16_swap_b32_e32 v219, v220
	v_add_f32_e32 v219, v219, v220
	v_mov_b32_e32 v220, v219
	s_nop 1
	v_permlane32_swap_b32_e32 v219, v220
	s_and_saveexec_b64 s[24:25], s[0:1]
	v_add_f32_e32 v219, v219, v220
	ds_write_b32 v218, v219 offset:2304
	s_or_b64 exec, exec, s[24:25]
	v_fma_f32 v219, v30, v30, 0
	v_fmac_f32_e32 v219, v31, v31
	v_fmac_f32_e32 v219, v32, v32
	v_fmac_f32_e32 v219, v33, v33
	v_fmac_f32_e32 v219, v18, v18
	v_fmac_f32_e32 v219, v19, v19
	v_fmac_f32_e32 v219, v20, v20
	v_fmac_f32_e32 v219, v21, v21
	v_mov_b32_e32 v220, v219
	s_nop 1
	v_permlane16_swap_b32_e32 v219, v220
	v_add_f32_e32 v219, v219, v220
	v_mov_b32_e32 v220, v219
	s_nop 1
	v_permlane32_swap_b32_e32 v219, v220
	s_and_saveexec_b64 s[24:25], s[0:1]
	v_add_f32_e32 v219, v219, v220
	ds_write_b32 v218, v219 offset:2560
	s_or_b64 exec, exec, s[24:25]
	v_fma_f32 v219, v14, v14, 0
	v_fmac_f32_e32 v219, v15, v15
	v_fmac_f32_e32 v219, v16, v16
	v_fmac_f32_e32 v219, v17, v17
	v_fmac_f32_e32 v219, v2, v2
	v_fmac_f32_e32 v219, v3, v3
	v_fmac_f32_e32 v219, v4, v4
	v_fmac_f32_e32 v219, v5, v5
	v_mov_b32_e32 v220, v219
	s_nop 1
	v_permlane16_swap_b32_e32 v219, v220
	v_add_f32_e32 v219, v219, v220
	v_mov_b32_e32 v220, v219
	s_nop 1
	v_permlane32_swap_b32_e32 v219, v220
	s_and_saveexec_b64 s[24:25], s[0:1]
	v_add_f32_e32 v219, v219, v220
	ds_write_b32 v218, v219 offset:2816
	s_or_b64 exec, exec, s[24:25]
	v_fma_f32 v218, v126, v126, 0
	v_fmac_f32_e32 v218, v127, v127
	v_fmac_f32_e32 v218, v128, v128
	v_fmac_f32_e32 v218, v129, v129
	v_fmac_f32_e32 v218, v118, v118
	v_fmac_f32_e32 v218, v119, v119
	v_fmac_f32_e32 v218, v120, v120
	v_fmac_f32_e32 v218, v121, v121
	v_mov_b32_e32 v219, v218
	s_nop 1
	v_permlane16_swap_b32_e32 v218, v219
	v_add_f32_e32 v218, v218, v219
	v_or_b32_e32 v220, 0x100, v217
	v_mov_b32_e32 v219, v218
	s_nop 1
	v_permlane32_swap_b32_e32 v218, v219
	v_lshl_add_u32 v207, v220, 4, v207
	s_and_saveexec_b64 s[24:25], s[0:1]
	v_add_f32_e32 v218, v218, v219
	ds_write_b32 v207, v218
	s_or_b64 exec, exec, s[24:25]
	v_fma_f32 v218, v110, v110, 0
	v_fmac_f32_e32 v218, v111, v111
	v_fmac_f32_e32 v218, v112, v112
	v_fmac_f32_e32 v218, v113, v113
	v_fmac_f32_e32 v218, v106, v106
	v_fmac_f32_e32 v218, v107, v107
	v_fmac_f32_e32 v218, v108, v108
	v_fmac_f32_e32 v218, v109, v109
	v_mov_b32_e32 v219, v218
	s_nop 1
	v_permlane16_swap_b32_e32 v218, v219
	v_add_f32_e32 v218, v218, v219
	v_mov_b32_e32 v219, v218
	s_nop 1
	v_permlane32_swap_b32_e32 v218, v219
	s_and_saveexec_b64 s[24:25], s[0:1]
	v_add_f32_e32 v218, v218, v219
	ds_write_b32 v207, v218 offset:256
	s_or_b64 exec, exec, s[24:25]
	v_fma_f32 v218, v94, v94, 0
	v_fmac_f32_e32 v218, v95, v95
	v_fmac_f32_e32 v218, v96, v96
	v_fmac_f32_e32 v218, v97, v97
	v_fmac_f32_e32 v218, v90, v90
	v_fmac_f32_e32 v218, v91, v91
	v_fmac_f32_e32 v218, v92, v92
	v_fmac_f32_e32 v218, v93, v93
	v_mov_b32_e32 v219, v218
	s_nop 1
	v_permlane16_swap_b32_e32 v218, v219
	v_add_f32_e32 v218, v218, v219
	v_mov_b32_e32 v219, v218
	s_nop 1
	v_permlane32_swap_b32_e32 v218, v219
	s_and_saveexec_b64 s[24:25], s[0:1]
	v_add_f32_e32 v218, v218, v219
	ds_write_b32 v207, v218 offset:512
	s_or_b64 exec, exec, s[24:25]
	v_fma_f32 v218, v78, v78, 0
	v_fmac_f32_e32 v218, v79, v79
	v_fmac_f32_e32 v218, v80, v80
	v_fmac_f32_e32 v218, v81, v81
	v_fmac_f32_e32 v218, v74, v74
	v_fmac_f32_e32 v218, v75, v75
	v_fmac_f32_e32 v218, v76, v76
	v_fmac_f32_e32 v218, v77, v77
	v_mov_b32_e32 v219, v218
	s_nop 1
	v_permlane16_swap_b32_e32 v218, v219
	v_add_f32_e32 v218, v218, v219
	v_mov_b32_e32 v219, v218
	s_nop 1
	v_permlane32_swap_b32_e32 v218, v219
	s_and_saveexec_b64 s[24:25], s[0:1]
	v_add_f32_e32 v218, v218, v219
	ds_write_b32 v207, v218 offset:768
	s_or_b64 exec, exec, s[24:25]
	v_fma_f32 v218, v62, v62, 0
	v_fmac_f32_e32 v218, v63, v63
	v_fmac_f32_e32 v218, v64, v64
	v_fmac_f32_e32 v218, v65, v65
	v_fmac_f32_e32 v218, v54, v54
	v_fmac_f32_e32 v218, v55, v55
	v_fmac_f32_e32 v218, v56, v56
	v_fmac_f32_e32 v218, v57, v57
	v_mov_b32_e32 v219, v218
	s_nop 1
	v_permlane16_swap_b32_e32 v218, v219
	v_add_f32_e32 v218, v218, v219
	v_mov_b32_e32 v219, v218
	s_nop 1
	v_permlane32_swap_b32_e32 v218, v219
	s_and_saveexec_b64 s[24:25], s[0:1]
	v_add_f32_e32 v218, v218, v219
	ds_write_b32 v207, v218 offset:2048
	s_or_b64 exec, exec, s[24:25]
	v_fma_f32 v218, v42, v42, 0
	v_fmac_f32_e32 v218, v43, v43
	v_fmac_f32_e32 v218, v44, v44
	v_fmac_f32_e32 v218, v45, v45
	v_fmac_f32_e32 v218, v38, v38
	v_fmac_f32_e32 v218, v39, v39
	v_fmac_f32_e32 v218, v40, v40
	v_fmac_f32_e32 v218, v41, v41
	v_mov_b32_e32 v219, v218
	s_nop 1
	v_permlane16_swap_b32_e32 v218, v219
	v_add_f32_e32 v218, v218, v219
	v_mov_b32_e32 v219, v218
	s_nop 1
	v_permlane32_swap_b32_e32 v218, v219
	s_and_saveexec_b64 s[24:25], s[0:1]
	v_add_f32_e32 v218, v218, v219
	ds_write_b32 v207, v218 offset:2304
	s_or_b64 exec, exec, s[24:25]
	v_fma_f32 v218, v26, v26, 0
	v_fmac_f32_e32 v218, v27, v27
	v_fmac_f32_e32 v218, v28, v28
	v_fmac_f32_e32 v218, v29, v29
	v_fmac_f32_e32 v218, v22, v22
	v_fmac_f32_e32 v218, v23, v23
	v_fmac_f32_e32 v218, v24, v24
	v_fmac_f32_e32 v218, v25, v25
	v_mov_b32_e32 v219, v218
	s_nop 1
	v_permlane16_swap_b32_e32 v218, v219
	v_add_f32_e32 v218, v218, v219
	v_mov_b32_e32 v219, v218
	s_nop 1
	v_permlane32_swap_b32_e32 v218, v219
	s_and_saveexec_b64 s[24:25], s[0:1]
	v_add_f32_e32 v218, v218, v219
	ds_write_b32 v207, v218 offset:2560
	s_or_b64 exec, exec, s[24:25]
	v_fma_f32 v218, v10, v10, 0
	v_fmac_f32_e32 v218, v11, v11
	v_fmac_f32_e32 v218, v12, v12
	v_fmac_f32_e32 v218, v13, v13
	v_fmac_f32_e32 v218, v6, v6
	v_fmac_f32_e32 v218, v7, v7
	v_fmac_f32_e32 v218, v8, v8
	v_fmac_f32_e32 v218, v9, v9
	v_mov_b32_e32 v219, v218
	s_nop 1
	v_permlane16_swap_b32_e32 v218, v219
	v_add_f32_e32 v218, v218, v219
	v_mov_b32_e32 v219, v218
	s_nop 1
	v_permlane32_swap_b32_e32 v218, v219
	s_and_saveexec_b64 s[24:25], s[0:1]
	v_add_f32_e32 v218, v218, v219
	ds_write_b32 v207, v218 offset:2816
	s_or_b64 exec, exec, s[24:25]
	v_mov_b32_e32 v207, 0x3e0293ee
	v_cndmask_b32_e32 v224, 1.0, v207, vcc
	v_lshl_add_u32 v207, v217, 4, 0
	v_add_u32_e32 v218, 0x21000, v207
	s_waitcnt lgkmcnt(0)
	s_barrier
	ds_read_b128 v[220:223], v218
	s_waitcnt vmcnt(0)
	v_pk_mul_f32 v[200:201], v[224:225], v[200:201] op_sel_hi:[0,1]
	v_pk_mul_f32 v[198:199], v[224:225], v[198:199] op_sel_hi:[0,1]
	v_pk_mul_f32 v[196:197], v[224:225], v[196:197] op_sel_hi:[0,1]
	v_pk_mul_f32 v[194:195], v[224:225], v[194:195] op_sel_hi:[0,1]
	ds_read_b128 v[224:227], v218 offset:4096
	s_waitcnt lgkmcnt(1)
	v_add_f32_e32 v219, v220, v221
	v_add_f32_e32 v219, v222, v219
	v_add_f32_e32 v220, v223, v219
	v_mov_b32_e32 v219, 0x322bcc77
	v_fmamk_f32 v220, v220, 0x3c000000, v219
	v_rsq_f32_e32 v222, v220
	s_waitcnt lgkmcnt(0)
	v_add_f32_e32 v220, v224, v225
	v_add_u32_e32 v205, s22, v205
	v_add_f32_e32 v220, v226, v220
	v_mul_u32_u24_e32 v223, 0x210, v217
	s_movk_i32 s0, 0x7c0
	v_add_f32_e32 v220, v227, v220
	v_and_or_b32 v225, v205, s0, v204
	v_pk_mul_f32 v[204:205], v[122:123], v[222:223] op_sel_hi:[1,0]
	v_fmamk_f32 v220, v220, 0x3c000000, v219
	v_pk_mul_f32 v[204:205], v[198:199], v[204:205]
	v_rsq_f32_e32 v224, v220
	v_pk_mul_f32 v[220:221], v[190:191], v[204:205]
	v_pk_mul_f32 v[204:205], v[192:193], v[204:205]
	v_add_f32_e32 v226, v220, v221
	v_add_f32_e32 v227, v204, v205
	v_pk_mul_f32 v[204:205], v[124:125], v[222:223] op_sel_hi:[1,0]
	v_lshlrev_b32_e32 v207, 1, v206
	v_pk_mul_f32 v[204:205], v[200:201], v[204:205]
	s_mov_b64 s[0:1], 0x4000
	v_pk_mul_f32 v[220:221], v[186:187], v[204:205]
	v_pk_mul_f32 v[204:205], v[188:189], v[204:205]
	v_add_f32_e32 v220, v220, v221
	v_add_f32_e32 v205, v204, v205
	v_cvt_pk_f16_f32 v204, v226, v227
	v_cvt_pk_f16_f32 v205, v220, v205
	v_add3_u32 v220, 0, v223, v207
	ds_write_b64 v220, v[204:205]
	v_pk_mul_f32 v[204:205], v[126:127], v[224:225] op_sel_hi:[1,0]
	s_nop 0
	v_pk_mul_f32 v[204:205], v[198:199], v[204:205]
	s_nop 0
	v_pk_mul_f32 v[190:191], v[190:191], v[204:205]
	s_nop 0
	v_add_f32_e32 v207, v190, v191
	v_pk_mul_f32 v[190:191], v[192:193], v[204:205]
	v_mov_b32_e32 v205, 0
	v_add_f32_e32 v192, v190, v191
	v_pk_mul_f32 v[190:191], v[128:129], v[224:225] op_sel_hi:[1,0]
	s_nop 0
	v_pk_mul_f32 v[190:191], v[200:201], v[190:191]
	s_nop 0
	v_pk_mul_f32 v[186:187], v[186:187], v[190:191]
	s_nop 0
	v_add_f32_e32 v193, v186, v187
	v_pk_mul_f32 v[186:187], v[188:189], v[190:191]
	s_nop 0
	v_add_f32_e32 v187, v186, v187
	v_cvt_pk_f16_f32 v186, v207, v192
	v_cvt_pk_f16_f32 v187, v193, v187
	ds_write_b64 v220, v[186:187] offset:256
	v_lshlrev_b32_e32 v186, 3, v206
	v_pk_mul_f32 v[206:207], v[114:115], v[222:223] op_sel_hi:[1,0]
	v_lshl_or_b32 v204, v225, 10, v186
	v_pk_mul_f32 v[206:207], v[194:195], v[206:207]
	global_load_dwordx4 v[186:189], v204, s[16:17] offset:16
	global_load_dwordx4 v[190:193], v204, s[16:17]
	v_pk_mul_f32 v[226:227], v[182:183], v[206:207]
	v_pk_mul_f32 v[206:207], v[184:185], v[206:207]
	v_add_f32_e32 v221, v226, v227
	v_add_f32_e32 v225, v206, v207
	v_pk_mul_f32 v[206:207], v[116:117], v[222:223] op_sel_hi:[1,0]
	s_nop 0
	v_pk_mul_f32 v[206:207], v[196:197], v[206:207]
	s_nop 0
	v_pk_mul_f32 v[222:223], v[178:179], v[206:207]
	v_pk_mul_f32 v[206:207], v[180:181], v[206:207]
	v_add_f32_e32 v222, v222, v223
	v_add_f32_e32 v207, v206, v207
	v_cvt_pk_f16_f32 v206, v221, v225
	v_cvt_pk_f16_f32 v207, v222, v207
	ds_write_b64 v220, v[206:207] offset:32
	v_pk_mul_f32 v[206:207], v[118:119], v[224:225] op_sel_hi:[1,0]
	s_nop 0
	v_pk_mul_f32 v[206:207], v[194:195], v[206:207]
	s_nop 0
	v_pk_mul_f32 v[182:183], v[182:183], v[206:207]
	s_nop 0
	v_add_f32_e32 v221, v182, v183
	v_pk_mul_f32 v[182:183], v[184:185], v[206:207]
	v_lshl_add_u64 v[206:207], s[16:17], 0, v[204:205]
	v_add_f32_e32 v184, v182, v183
	v_pk_mul_f32 v[182:183], v[120:121], v[224:225] op_sel_hi:[1,0]
	s_nop 0
	v_pk_mul_f32 v[182:183], v[196:197], v[182:183]
	s_nop 0
	v_pk_mul_f32 v[178:179], v[178:179], v[182:183]
	s_nop 0
	v_add_f32_e32 v185, v178, v179
	v_pk_mul_f32 v[178:179], v[180:181], v[182:183]
	s_nop 0
	v_add_f32_e32 v179, v178, v179
	v_cvt_pk_f16_f32 v178, v221, v184
	v_cvt_pk_f16_f32 v179, v185, v179
	ds_write_b64 v220, v[178:179] offset:288
	ds_read_b128 v[222:225], v218 offset:256
	global_load_dwordx4 v[178:181], v204, s[16:17] offset:144
	global_load_dwordx4 v[182:185], v204, s[16:17] offset:128
	ds_read_b128 v[226:229], v218 offset:4352
	s_waitcnt lgkmcnt(1)
	v_add_f32_e32 v204, v222, v223
	v_add_f32_e32 v204, v224, v204
	v_add_f32_e32 v204, v225, v204
	v_fmamk_f32 v204, v204, 0x3c000000, v219
	v_rsq_f32_e32 v222, v204
	s_waitcnt lgkmcnt(0)
	v_add_f32_e32 v204, v226, v227
	v_add_f32_e32 v204, v228, v204
	v_add_f32_e32 v204, v229, v204
	v_pk_mul_f32 v[226:227], v[102:103], v[222:223] op_sel_hi:[1,0]
	v_fmamk_f32 v204, v204, 0x3c000000, v219
	v_pk_mul_f32 v[226:227], v[198:199], v[226:227]
	v_rsq_f32_e32 v224, v204
	v_pk_mul_f32 v[228:229], v[174:175], v[226:227]
	v_pk_mul_f32 v[226:227], v[176:177], v[226:227]
	v_add_f32_e32 v204, v228, v229
	v_add_f32_e32 v221, v226, v227
	v_pk_mul_f32 v[226:227], v[104:105], v[222:223] op_sel_hi:[1,0]
	s_nop 0
	v_pk_mul_f32 v[226:227], v[200:201], v[226:227]
	s_nop 0
	v_pk_mul_f32 v[228:229], v[170:171], v[226:227]
	v_pk_mul_f32 v[226:227], v[172:173], v[226:227]
	v_add_f32_e32 v223, v228, v229
	v_add_f32_e32 v225, v226, v227
	v_cvt_pk_f16_f32 v226, v204, v221
	v_cvt_pk_f16_f32 v227, v223, v225
	ds_write_b64 v220, v[226:227] offset:8448
	v_pk_mul_f32 v[226:227], v[110:111], v[224:225] op_sel_hi:[1,0]
	v_pk_mul_f32 v[228:229], v[98:99], v[222:223] op_sel_hi:[1,0]
	v_pk_mul_f32 v[226:227], v[198:199], v[226:227]
	v_pk_mul_f32 v[228:229], v[194:195], v[228:229]
	v_pk_mul_f32 v[174:175], v[174:175], v[226:227]
	v_pk_mul_f32 v[222:223], v[100:101], v[222:223] op_sel_hi:[1,0]
	v_add_f32_e32 v221, v174, v175
	v_pk_mul_f32 v[174:175], v[176:177], v[226:227]
	v_pk_mul_f32 v[230:231], v[166:167], v[228:229]
	v_add_f32_e32 v176, v174, v175
	v_pk_mul_f32 v[174:175], v[112:113], v[224:225] op_sel_hi:[1,0]
	v_pk_mul_f32 v[228:229], v[168:169], v[228:229]
	v_pk_mul_f32 v[174:175], v[200:201], v[174:175]
	v_pk_mul_f32 v[222:223], v[196:197], v[222:223]
	v_pk_mul_f32 v[170:171], v[170:171], v[174:175]
	v_add_f32_e32 v225, v228, v229
	v_add_f32_e32 v177, v170, v171
	v_pk_mul_f32 v[170:171], v[172:173], v[174:175]
	v_pk_mul_f32 v[228:229], v[162:163], v[222:223]
	v_add_f32_e32 v171, v170, v171
	v_cvt_pk_f16_f32 v170, v221, v176
	v_cvt_pk_f16_f32 v171, v177, v171
	ds_write_b64 v220, v[170:171] offset:8704
	v_lshl_add_u64 v[170:171], v[206:207], 0, s[0:1]
	s_movk_i32 s0, 0x4000
	v_add_co_u32_e64 v226, s[0:1], s0, v206
	v_pk_mul_f32 v[222:223], v[164:165], v[222:223]
	s_nop 0
	v_addc_co_u32_e64 v227, s[0:1], 0, v207, s[0:1]
	v_add_f32_e32 v223, v222, v223
	global_load_dwordx4 v[174:177], v[226:227], off
	s_nop 0
	global_load_dwordx4 v[170:173], v[170:171], off offset:16
	v_add_f32_e32 v221, v230, v231
	v_add_f32_e32 v228, v228, v229
	v_cvt_pk_f16_f32 v222, v221, v225
	v_cvt_pk_f16_f32 v223, v228, v223
	ds_write_b64 v220, v[222:223] offset:8480
	v_pk_mul_f32 v[222:223], v[106:107], v[224:225] op_sel_hi:[1,0]
	s_mov_b64 s[0:1], 0x4080
	v_pk_mul_f32 v[222:223], v[194:195], v[222:223]
	v_add_u32_e32 v204, 0x2100, v220
	v_pk_mul_f32 v[166:167], v[166:167], v[222:223]
	s_nop 0
	v_add_f32_e32 v221, v166, v167
	v_pk_mul_f32 v[166:167], v[168:169], v[222:223]
	s_nop 0
	v_add_f32_e32 v168, v166, v167
	v_pk_mul_f32 v[166:167], v[108:109], v[224:225] op_sel_hi:[1,0]
	s_nop 0
	v_pk_mul_f32 v[166:167], v[196:197], v[166:167]
	s_nop 0
	v_pk_mul_f32 v[162:163], v[162:163], v[166:167]
	s_nop 0
	v_add_f32_e32 v169, v162, v163
	v_pk_mul_f32 v[162:163], v[164:165], v[166:167]
	s_nop 0
	v_add_f32_e32 v163, v162, v163
	v_cvt_pk_f16_f32 v162, v221, v168
	v_cvt_pk_f16_f32 v163, v169, v163
	ds_write_b64 v220, v[162:163] offset:8736
	ds_read_b128 v[222:225], v218 offset:512
	v_lshl_add_u64 v[162:163], v[206:207], 0, s[0:1]
	global_load_dwordx4 v[166:169], v[226:227], off offset:128
	s_nop 0
	global_load_dwordx4 v[162:165], v[162:163], off offset:16
	ds_read_b128 v[226:229], v218 offset:4608
	s_mov_b64 s[0:1], 0x8000
	s_waitcnt lgkmcnt(1)
	v_add_f32_e32 v221, v222, v223
	v_add_f32_e32 v221, v224, v221
	v_add_f32_e32 v221, v225, v221
	v_fmamk_f32 v221, v221, 0x3c000000, v219
	v_rsq_f32_e32 v222, v221
	s_waitcnt lgkmcnt(0)
	v_add_f32_e32 v221, v226, v227
	v_add_f32_e32 v221, v228, v221
	v_add_f32_e32 v221, v229, v221
	v_pk_mul_f32 v[226:227], v[86:87], v[222:223] op_sel_hi:[1,0]
	v_fmamk_f32 v221, v221, 0x3c000000, v219
	v_pk_mul_f32 v[226:227], v[198:199], v[226:227]
	v_rsq_f32_e32 v224, v221
	v_pk_mul_f32 v[228:229], v[158:159], v[226:227]
	v_pk_mul_f32 v[226:227], v[160:161], v[226:227]
	v_add_f32_e32 v221, v228, v229
	v_add_f32_e32 v223, v226, v227
	v_pk_mul_f32 v[226:227], v[88:89], v[222:223] op_sel_hi:[1,0]
	s_nop 0
	v_pk_mul_f32 v[226:227], v[200:201], v[226:227]
	s_nop 0
	v_pk_mul_f32 v[228:229], v[154:155], v[226:227]
	v_pk_mul_f32 v[226:227], v[156:157], v[226:227]
	v_add_f32_e32 v225, v228, v229
	v_add_f32_e32 v227, v226, v227
	v_cvt_pk_f16_f32 v226, v221, v223
	v_cvt_pk_f16_f32 v227, v225, v227
	ds_write_b64 v220, v[226:227] offset:16896
	v_pk_mul_f32 v[226:227], v[94:95], v[224:225] op_sel_hi:[1,0]
	v_pk_mul_f32 v[228:229], v[82:83], v[222:223] op_sel_hi:[1,0]
	v_pk_mul_f32 v[226:227], v[198:199], v[226:227]
	v_pk_mul_f32 v[228:229], v[194:195], v[228:229]
	v_pk_mul_f32 v[158:159], v[158:159], v[226:227]
	v_pk_mul_f32 v[222:223], v[84:85], v[222:223] op_sel_hi:[1,0]
	v_add_f32_e32 v221, v158, v159
	v_pk_mul_f32 v[158:159], v[160:161], v[226:227]
	v_pk_mul_f32 v[230:231], v[150:151], v[228:229]
	v_add_f32_e32 v160, v158, v159
	v_pk_mul_f32 v[158:159], v[96:97], v[224:225] op_sel_hi:[1,0]
	v_pk_mul_f32 v[228:229], v[152:153], v[228:229]
	v_pk_mul_f32 v[158:159], v[200:201], v[158:159]
	v_pk_mul_f32 v[222:223], v[196:197], v[222:223]
	v_pk_mul_f32 v[154:155], v[154:155], v[158:159]
	v_add_f32_e32 v225, v228, v229
	v_add_f32_e32 v161, v154, v155
	v_pk_mul_f32 v[154:155], v[156:157], v[158:159]
	v_pk_mul_f32 v[228:229], v[146:147], v[222:223]
	v_add_f32_e32 v155, v154, v155
	v_cvt_pk_f16_f32 v154, v221, v160
	v_cvt_pk_f16_f32 v155, v161, v155
	ds_write_b64 v220, v[154:155] offset:17152
	v_lshl_add_u64 v[154:155], v[206:207], 0, s[0:1]
	s_mov_b32 s0, 0x8000
	v_add_co_u32_e64 v226, s[0:1], s0, v206
	v_pk_mul_f32 v[222:223], v[148:149], v[222:223]
	s_nop 0
	v_addc_co_u32_e64 v227, s[0:1], 0, v207, s[0:1]
	v_add_f32_e32 v223, v222, v223
	global_load_dwordx4 v[158:161], v[226:227], off
	s_nop 0
	global_load_dwordx4 v[154:157], v[154:155], off offset:16
	v_add_f32_e32 v221, v230, v231
	v_add_f32_e32 v228, v228, v229
	v_cvt_pk_f16_f32 v222, v221, v225
	v_cvt_pk_f16_f32 v223, v228, v223
	ds_write_b64 v220, v[222:223] offset:16928
	v_pk_mul_f32 v[222:223], v[90:91], v[224:225] op_sel_hi:[1,0]
	s_mov_b64 s[0:1], 0x8080
	v_pk_mul_f32 v[222:223], v[194:195], v[222:223]
	s_nop 0
	v_pk_mul_f32 v[150:151], v[150:151], v[222:223]
	s_nop 0
	v_add_f32_e32 v221, v150, v151
	v_pk_mul_f32 v[150:151], v[152:153], v[222:223]
	s_nop 0
	v_add_f32_e32 v152, v150, v151
	v_pk_mul_f32 v[150:151], v[92:93], v[224:225] op_sel_hi:[1,0]
	s_nop 0
	v_pk_mul_f32 v[150:151], v[196:197], v[150:151]
	s_nop 0
	v_pk_mul_f32 v[146:147], v[146:147], v[150:151]
	s_nop 0
	v_add_f32_e32 v153, v146, v147
	v_pk_mul_f32 v[146:147], v[148:149], v[150:151]
	s_nop 0
	v_add_f32_e32 v147, v146, v147
	v_cvt_pk_f16_f32 v146, v221, v152
	v_cvt_pk_f16_f32 v147, v153, v147
	ds_write_b64 v220, v[146:147] offset:17184
	ds_read_b128 v[222:225], v218 offset:768
	v_lshl_add_u64 v[146:147], v[206:207], 0, s[0:1]
	global_load_dwordx4 v[150:153], v[226:227], off offset:128
	s_nop 0
	global_load_dwordx4 v[146:149], v[146:147], off offset:16
	ds_read_b128 v[226:229], v218 offset:4864
	s_mov_b64 s[0:1], 0xc000
	s_waitcnt lgkmcnt(1)
	v_add_f32_e32 v221, v222, v223
	v_add_f32_e32 v221, v224, v221
	v_add_f32_e32 v221, v225, v221
	v_fmamk_f32 v221, v221, 0x3c000000, v219
	v_rsq_f32_e32 v222, v221
	s_waitcnt lgkmcnt(0)
	v_add_f32_e32 v221, v226, v227
	v_add_f32_e32 v221, v228, v221
	v_add_f32_e32 v221, v229, v221
	v_pk_mul_f32 v[226:227], v[70:71], v[222:223] op_sel_hi:[1,0]
	v_fmamk_f32 v221, v221, 0x3c000000, v219
	v_pk_mul_f32 v[226:227], v[198:199], v[226:227]
	v_rsq_f32_e32 v224, v221
	v_pk_mul_f32 v[228:229], v[142:143], v[226:227]
	v_pk_mul_f32 v[226:227], v[144:145], v[226:227]
	v_add_f32_e32 v221, v228, v229
	v_add_f32_e32 v223, v226, v227
	v_pk_mul_f32 v[226:227], v[72:73], v[222:223] op_sel_hi:[1,0]
	s_nop 0
	v_pk_mul_f32 v[226:227], v[200:201], v[226:227]
	s_nop 0
	v_pk_mul_f32 v[228:229], v[138:139], v[226:227]
	v_pk_mul_f32 v[226:227], v[140:141], v[226:227]
	v_add_f32_e32 v225, v228, v229
	v_add_f32_e32 v227, v226, v227
	v_cvt_pk_f16_f32 v226, v221, v223
	v_cvt_pk_f16_f32 v227, v225, v227
	ds_write_b64 v220, v[226:227] offset:25344
	v_pk_mul_f32 v[226:227], v[78:79], v[224:225] op_sel_hi:[1,0]
	v_pk_mul_f32 v[228:229], v[58:59], v[222:223] op_sel_hi:[1,0]
	v_pk_mul_f32 v[226:227], v[198:199], v[226:227]
	v_pk_mul_f32 v[228:229], v[194:195], v[228:229]
	v_pk_mul_f32 v[142:143], v[142:143], v[226:227]
	v_pk_mul_f32 v[222:223], v[60:61], v[222:223] op_sel_hi:[1,0]
	v_add_f32_e32 v221, v142, v143
	v_pk_mul_f32 v[142:143], v[144:145], v[226:227]
	v_pk_mul_f32 v[230:231], v[134:135], v[228:229]
	v_add_f32_e32 v144, v142, v143
	v_pk_mul_f32 v[142:143], v[80:81], v[224:225] op_sel_hi:[1,0]
	v_pk_mul_f32 v[228:229], v[136:137], v[228:229]
	v_pk_mul_f32 v[142:143], v[200:201], v[142:143]
	v_pk_mul_f32 v[222:223], v[196:197], v[222:223]
	v_pk_mul_f32 v[138:139], v[138:139], v[142:143]
	v_add_f32_e32 v225, v228, v229
	v_add_f32_e32 v145, v138, v139
	v_pk_mul_f32 v[138:139], v[140:141], v[142:143]
	v_pk_mul_f32 v[228:229], v[130:131], v[222:223]
	v_add_f32_e32 v139, v138, v139
	v_cvt_pk_f16_f32 v138, v221, v144
	v_cvt_pk_f16_f32 v139, v145, v139
	ds_write_b64 v220, v[138:139] offset:25600
	v_lshl_add_u64 v[138:139], v[206:207], 0, s[0:1]
	s_mov_b32 s0, 0xc000
	v_add_co_u32_e64 v226, s[0:1], s0, v206
	v_pk_mul_f32 v[222:223], v[132:133], v[222:223]
	s_nop 0
	v_addc_co_u32_e64 v227, s[0:1], 0, v207, s[0:1]
	v_add_f32_e32 v223, v222, v223
	global_load_dwordx4 v[142:145], v[226:227], off
	s_nop 0
	global_load_dwordx4 v[138:141], v[138:139], off offset:16
	v_add_f32_e32 v221, v230, v231
	v_add_f32_e32 v228, v228, v229
	v_cvt_pk_f16_f32 v222, v221, v225
	v_cvt_pk_f16_f32 v223, v228, v223
	ds_write_b64 v220, v[222:223] offset:25376
	v_pk_mul_f32 v[222:223], v[74:75], v[224:225] op_sel_hi:[1,0]
	s_mov_b64 s[0:1], 0xc080
	v_pk_mul_f32 v[222:223], v[194:195], v[222:223]
	s_nop 0
	v_pk_mul_f32 v[134:135], v[134:135], v[222:223]
	s_nop 0
	v_add_f32_e32 v221, v134, v135
	v_pk_mul_f32 v[134:135], v[136:137], v[222:223]
	s_nop 0
	v_add_f32_e32 v136, v134, v135
	v_pk_mul_f32 v[134:135], v[76:77], v[224:225] op_sel_hi:[1,0]
	s_nop 0
	v_pk_mul_f32 v[134:135], v[196:197], v[134:135]
	s_nop 0
	v_pk_mul_f32 v[130:131], v[130:131], v[134:135]
	s_nop 0
	v_add_f32_e32 v137, v130, v131
	v_pk_mul_f32 v[130:131], v[132:133], v[134:135]
	s_nop 0
	v_add_f32_e32 v131, v130, v131
	v_cvt_pk_f16_f32 v130, v221, v136
	v_cvt_pk_f16_f32 v131, v137, v131
	ds_write_b64 v220, v[130:131] offset:25632
	ds_read_b128 v[222:225], v218 offset:2048
	v_lshl_add_u64 v[130:131], v[206:207], 0, s[0:1]
	global_load_dwordx4 v[134:137], v[226:227], off offset:128
	s_nop 0
	global_load_dwordx4 v[130:133], v[130:131], off offset:16
	ds_read_b128 v[226:229], v218 offset:6144
	s_and_b64 s[0:1], vcc, exec
	s_waitcnt lgkmcnt(1)
	v_add_f32_e32 v206, v222, v223
	v_add_f32_e32 v206, v224, v206
	v_add_f32_e32 v206, v225, v206
	v_fmamk_f32 v206, v206, 0x3c000000, v219
	v_rsq_f32_e32 v206, v206
	s_waitcnt lgkmcnt(0)
	v_add_f32_e32 v207, v226, v227
	v_add_f32_e32 v207, v228, v207
	v_add_f32_e32 v207, v229, v207
	v_fmamk_f32 v207, v207, 0x3c000000, v219
	v_pk_mul_f32 v[224:225], v[66:67], v[206:207] op_sel_hi:[1,0]
	v_rsq_f32_e32 v222, v207
	v_pk_mul_f32 v[224:225], v[198:199], v[224:225]
	s_cselect_b32 s1, s7, s9
	s_waitcnt vmcnt(14)
	v_pk_mul_f32 v[226:227], v[190:191], v[224:225]
	v_pk_mul_f32 v[224:225], v[192:193], v[224:225]
	v_add_f32_e32 v207, v226, v227
	v_add_f32_e32 v221, v224, v225
	v_pk_mul_f32 v[224:225], v[68:69], v[206:207] op_sel_hi:[1,0]
	s_cselect_b32 s0, s6, s8
	v_pk_mul_f32 v[224:225], v[200:201], v[224:225]
	s_lshl_b32 s3, s3, 1
	v_pk_mul_f32 v[226:227], v[186:187], v[224:225]
	v_pk_mul_f32 v[224:225], v[188:189], v[224:225]
	v_add_f32_e32 v223, v226, v227
	v_add_f32_e32 v225, v224, v225
	v_cvt_pk_f16_f32 v224, v207, v221
	v_cvt_pk_f16_f32 v225, v223, v225
	ds_write_b64 v204, v[224:225] offset:59136
	v_pk_mul_f32 v[224:225], v[62:63], v[222:223] op_sel_hi:[1,0]
	s_and_b32 s3, s3, 0x1ffff0
	v_pk_mul_f32 v[224:225], v[198:199], v[224:225]
	s_or_b32 s3, s3, s21
	v_pk_mul_f32 v[190:191], v[190:191], v[224:225]
	s_nop 0
	v_add_f32_e32 v207, v190, v191
	v_pk_mul_f32 v[190:191], v[192:193], v[224:225]
	s_nop 0
	v_add_f32_e32 v192, v190, v191
	v_pk_mul_f32 v[190:191], v[64:65], v[222:223] op_sel_hi:[1,0]
	s_nop 0
	v_pk_mul_f32 v[190:191], v[200:201], v[190:191]
	s_nop 0
	v_pk_mul_f32 v[186:187], v[186:187], v[190:191]
	s_nop 0
	v_add_f32_e32 v193, v186, v187
	v_pk_mul_f32 v[186:187], v[188:189], v[190:191]
	s_nop 0
	v_add_f32_e32 v187, v186, v187
	v_cvt_pk_f16_f32 v186, v207, v192
	v_cvt_pk_f16_f32 v187, v193, v187
	ds_write_b64 v204, v[186:187] offset:59392
	v_pk_mul_f32 v[186:187], v[50:51], v[206:207] op_sel_hi:[1,0]
	s_nop 0
	v_pk_mul_f32 v[186:187], v[194:195], v[186:187]
	s_waitcnt vmcnt(12)
	v_pk_mul_f32 v[188:189], v[182:183], v[186:187]
	v_pk_mul_f32 v[186:187], v[184:185], v[186:187]
	v_add_f32_e32 v190, v188, v189
	v_add_f32_e32 v191, v186, v187
	v_pk_mul_f32 v[186:187], v[52:53], v[206:207] op_sel_hi:[1,0]
	s_nop 0
	v_pk_mul_f32 v[186:187], v[196:197], v[186:187]
	s_nop 0
	v_pk_mul_f32 v[188:189], v[178:179], v[186:187]
	v_pk_mul_f32 v[186:187], v[180:181], v[186:187]
	v_add_f32_e32 v188, v188, v189
	v_add_f32_e32 v187, v186, v187
	v_cvt_pk_f16_f32 v186, v190, v191
	v_cvt_pk_f16_f32 v187, v188, v187
	ds_write_b64 v204, v[186:187] offset:59168
	v_pk_mul_f32 v[186:187], v[54:55], v[222:223] op_sel_hi:[1,0]
	s_nop 0
	v_pk_mul_f32 v[186:187], v[194:195], v[186:187]
	s_nop 0
	v_pk_mul_f32 v[182:183], v[182:183], v[186:187]
	s_nop 0
	v_add_f32_e32 v188, v182, v183
	v_pk_mul_f32 v[182:183], v[184:185], v[186:187]
	v_add_u32_e32 v186, 0x4200, v220
	v_add_f32_e32 v184, v182, v183
	v_pk_mul_f32 v[182:183], v[56:57], v[222:223] op_sel_hi:[1,0]
	s_nop 0
	v_pk_mul_f32 v[182:183], v[196:197], v[182:183]
	s_nop 0
	v_pk_mul_f32 v[178:179], v[178:179], v[182:183]
	s_nop 0
	v_add_f32_e32 v185, v178, v179
	v_pk_mul_f32 v[178:179], v[180:181], v[182:183]
	s_nop 0
	v_add_f32_e32 v179, v178, v179
	v_cvt_pk_f16_f32 v178, v188, v184
	v_cvt_pk_f16_f32 v179, v185, v179
	ds_write_b64 v204, v[178:179] offset:59424
	ds_read_b128 v[178:181], v218 offset:2304
	ds_read_b128 v[182:185], v218 offset:6400
	s_waitcnt lgkmcnt(1)
	v_add_f32_e32 v178, v178, v179
	v_add_f32_e32 v178, v180, v178
	v_add_f32_e32 v178, v181, v178
	v_fmamk_f32 v178, v178, 0x3c000000, v219
	v_rsq_f32_e32 v178, v178
	s_waitcnt lgkmcnt(0)
	v_add_f32_e32 v179, v182, v183
	v_add_f32_e32 v179, v184, v179
	v_add_f32_e32 v179, v185, v179
	v_fmamk_f32 v179, v179, 0x3c000000, v219
	v_pk_mul_f32 v[182:183], v[46:47], v[178:179] op_sel_hi:[1,0]
	v_rsq_f32_e32 v180, v179
	v_pk_mul_f32 v[182:183], v[198:199], v[182:183]
	s_waitcnt vmcnt(11)
	v_pk_mul_f32 v[184:185], v[174:175], v[182:183]
	v_pk_mul_f32 v[182:183], v[176:177], v[182:183]
	v_add_f32_e32 v179, v184, v185
	v_add_f32_e32 v181, v182, v183
	v_pk_mul_f32 v[182:183], v[48:49], v[178:179] op_sel_hi:[1,0]
	s_nop 0
	v_pk_mul_f32 v[182:183], v[200:201], v[182:183]
	s_waitcnt vmcnt(10)
	v_pk_mul_f32 v[184:185], v[170:171], v[182:183]
	v_pk_mul_f32 v[182:183], v[172:173], v[182:183]
	v_add_f32_e32 v184, v184, v185
	v_add_f32_e32 v183, v182, v183
	v_cvt_pk_f16_f32 v182, v179, v181
	v_cvt_pk_f16_f32 v183, v184, v183
	ds_write_b64 v186, v[182:183] offset:59136
	v_pk_mul_f32 v[182:183], v[42:43], v[180:181] op_sel_hi:[1,0]
	s_nop 0
	v_pk_mul_f32 v[182:183], v[198:199], v[182:183]
	s_nop 0
	v_pk_mul_f32 v[174:175], v[174:175], v[182:183]
	s_nop 0
	v_add_f32_e32 v179, v174, v175
	v_pk_mul_f32 v[174:175], v[176:177], v[182:183]
	s_nop 0
	v_add_f32_e32 v176, v174, v175
	v_pk_mul_f32 v[174:175], v[44:45], v[180:181] op_sel_hi:[1,0]
	s_nop 0
	v_pk_mul_f32 v[174:175], v[200:201], v[174:175]
	s_nop 0
	v_pk_mul_f32 v[170:171], v[170:171], v[174:175]
	s_nop 0
	v_add_f32_e32 v177, v170, v171
	v_pk_mul_f32 v[170:171], v[172:173], v[174:175]
	s_nop 0
	v_add_f32_e32 v171, v170, v171
	v_cvt_pk_f16_f32 v170, v179, v176
	v_cvt_pk_f16_f32 v171, v177, v171
	ds_write_b64 v186, v[170:171] offset:59392
	v_pk_mul_f32 v[170:171], v[34:35], v[178:179] op_sel_hi:[1,0]
	s_nop 0
	v_pk_mul_f32 v[170:171], v[194:195], v[170:171]
	s_waitcnt vmcnt(9)
	v_pk_mul_f32 v[172:173], v[166:167], v[170:171]
	v_pk_mul_f32 v[170:171], v[168:169], v[170:171]
	v_add_f32_e32 v174, v172, v173
	v_add_f32_e32 v175, v170, v171
	v_pk_mul_f32 v[170:171], v[36:37], v[178:179] op_sel_hi:[1,0]
	s_nop 0
	v_pk_mul_f32 v[170:171], v[196:197], v[170:171]
	s_waitcnt vmcnt(8)
	v_pk_mul_f32 v[172:173], v[162:163], v[170:171]
	v_pk_mul_f32 v[170:171], v[164:165], v[170:171]
	v_add_f32_e32 v172, v172, v173
	v_add_f32_e32 v171, v170, v171
	v_cvt_pk_f16_f32 v170, v174, v175
	v_cvt_pk_f16_f32 v171, v172, v171
	ds_write_b64 v186, v[170:171] offset:59168
	v_pk_mul_f32 v[170:171], v[38:39], v[180:181] op_sel_hi:[1,0]
	s_nop 0
	v_pk_mul_f32 v[170:171], v[194:195], v[170:171]
	s_nop 0
	v_pk_mul_f32 v[166:167], v[166:167], v[170:171]
	s_nop 0
	v_add_f32_e32 v172, v166, v167
	v_pk_mul_f32 v[166:167], v[168:169], v[170:171]
	v_add_u32_e32 v170, 0x6300, v220
	v_add_f32_e32 v168, v166, v167
	v_pk_mul_f32 v[166:167], v[40:41], v[180:181] op_sel_hi:[1,0]
	s_nop 0
	v_pk_mul_f32 v[166:167], v[196:197], v[166:167]
	s_nop 0
	v_pk_mul_f32 v[162:163], v[162:163], v[166:167]
	s_nop 0
	v_add_f32_e32 v169, v162, v163
	v_pk_mul_f32 v[162:163], v[164:165], v[166:167]
	s_nop 0
	v_add_f32_e32 v163, v162, v163
	v_cvt_pk_f16_f32 v162, v172, v168
	v_cvt_pk_f16_f32 v163, v169, v163
	ds_write_b64 v186, v[162:163] offset:59424
	ds_read_b128 v[162:165], v218 offset:2560
	ds_read_b128 v[166:169], v218 offset:6656
	s_waitcnt lgkmcnt(1)
	v_add_f32_e32 v162, v162, v163
	v_add_f32_e32 v162, v164, v162
	v_add_f32_e32 v162, v165, v162
	v_fmamk_f32 v162, v162, 0x3c000000, v219
	v_rsq_f32_e32 v162, v162
	s_waitcnt lgkmcnt(0)
	v_add_f32_e32 v163, v166, v167
	v_add_f32_e32 v163, v168, v163
	v_add_f32_e32 v163, v169, v163
	v_fmamk_f32 v163, v163, 0x3c000000, v219
	v_pk_mul_f32 v[166:167], v[30:31], v[162:163] op_sel_hi:[1,0]
	v_rsq_f32_e32 v164, v163
	v_pk_mul_f32 v[166:167], v[198:199], v[166:167]
	s_waitcnt vmcnt(7)
	v_pk_mul_f32 v[168:169], v[158:159], v[166:167]
	v_pk_mul_f32 v[166:167], v[160:161], v[166:167]
	v_add_f32_e32 v163, v168, v169
	v_add_f32_e32 v165, v166, v167
	v_pk_mul_f32 v[166:167], v[32:33], v[162:163] op_sel_hi:[1,0]
	s_nop 0
	v_pk_mul_f32 v[166:167], v[200:201], v[166:167]
	s_waitcnt vmcnt(6)
	v_pk_mul_f32 v[168:169], v[154:155], v[166:167]
	v_pk_mul_f32 v[166:167], v[156:157], v[166:167]
	v_add_f32_e32 v168, v168, v169
	v_add_f32_e32 v167, v166, v167
	v_cvt_pk_f16_f32 v166, v163, v165
	v_cvt_pk_f16_f32 v167, v168, v167
	ds_write_b64 v170, v[166:167] offset:59136
	v_pk_mul_f32 v[166:167], v[26:27], v[164:165] op_sel_hi:[1,0]
	s_nop 0
	v_pk_mul_f32 v[166:167], v[198:199], v[166:167]
	s_nop 0
	v_pk_mul_f32 v[158:159], v[158:159], v[166:167]
	s_nop 0
	v_add_f32_e32 v163, v158, v159
	v_pk_mul_f32 v[158:159], v[160:161], v[166:167]
	s_nop 0
	v_add_f32_e32 v160, v158, v159
	v_pk_mul_f32 v[158:159], v[28:29], v[164:165] op_sel_hi:[1,0]
	s_nop 0
	v_pk_mul_f32 v[158:159], v[200:201], v[158:159]
	s_nop 0
	v_pk_mul_f32 v[154:155], v[154:155], v[158:159]
	s_nop 0
	v_add_f32_e32 v161, v154, v155
	v_pk_mul_f32 v[154:155], v[156:157], v[158:159]
	s_nop 0
	v_add_f32_e32 v155, v154, v155
	v_cvt_pk_f16_f32 v154, v163, v160
	v_cvt_pk_f16_f32 v155, v161, v155
	ds_write_b64 v170, v[154:155] offset:59392
	v_pk_mul_f32 v[154:155], v[18:19], v[162:163] op_sel_hi:[1,0]
	s_nop 0
	v_pk_mul_f32 v[154:155], v[194:195], v[154:155]
	s_waitcnt vmcnt(5)
	v_pk_mul_f32 v[156:157], v[150:151], v[154:155]
	v_pk_mul_f32 v[154:155], v[152:153], v[154:155]
	v_add_f32_e32 v158, v156, v157
	v_add_f32_e32 v159, v154, v155
	v_pk_mul_f32 v[154:155], v[20:21], v[162:163] op_sel_hi:[1,0]
	s_nop 0
	v_pk_mul_f32 v[154:155], v[196:197], v[154:155]
	s_waitcnt vmcnt(4)
	v_pk_mul_f32 v[156:157], v[146:147], v[154:155]
	v_pk_mul_f32 v[154:155], v[148:149], v[154:155]
	v_add_f32_e32 v156, v156, v157
	v_add_f32_e32 v155, v154, v155
	v_cvt_pk_f16_f32 v154, v158, v159
	v_cvt_pk_f16_f32 v155, v156, v155
	ds_write_b64 v170, v[154:155] offset:59168
	v_pk_mul_f32 v[154:155], v[22:23], v[164:165] op_sel_hi:[1,0]
	s_nop 0
	v_pk_mul_f32 v[154:155], v[194:195], v[154:155]
	s_nop 0
	v_pk_mul_f32 v[150:151], v[150:151], v[154:155]
	s_nop 0
	v_add_f32_e32 v156, v150, v151
	v_pk_mul_f32 v[150:151], v[152:153], v[154:155]
	v_add_u32_e32 v154, 0xe700, v204
	v_add_f32_e32 v152, v150, v151
	v_pk_mul_f32 v[150:151], v[24:25], v[164:165] op_sel_hi:[1,0]
	v_lshlrev_b32_e32 v204, 1, v215
	v_pk_mul_f32 v[150:151], v[196:197], v[150:151]
	v_lshl_add_u64 v[166:167], s[0:1], 0, v[204:205]
	v_pk_mul_f32 v[146:147], v[146:147], v[150:151]
	s_lshl_b32 s0, s3, 11
	v_add_f32_e32 v153, v146, v147
	v_pk_mul_f32 v[146:147], v[148:149], v[150:151]
	s_or_b32 s0, s0, s23
	v_add_f32_e32 v147, v146, v147
	v_cvt_pk_f16_f32 v146, v156, v152
	v_cvt_pk_f16_f32 v147, v153, v147
	ds_write_b64 v170, v[146:147] offset:59424
	ds_read_b128 v[146:149], v218 offset:2816
	ds_read_b128 v[150:153], v218 offset:6912
	v_or_b32_e32 v168, s0, v213
	v_ashrrev_i32_e32 v169, 31, v168
	v_or_b32_e32 v170, s0, v211
	s_waitcnt lgkmcnt(1)
	v_add_f32_e32 v146, v146, v147
	v_add_f32_e32 v146, v148, v146
	v_add_f32_e32 v146, v149, v146
	v_fmamk_f32 v146, v146, 0x3c000000, v219
	v_rsq_f32_e32 v146, v146
	s_waitcnt lgkmcnt(0)
	v_add_f32_e32 v147, v150, v151
	v_add_f32_e32 v147, v152, v147
	v_add_f32_e32 v147, v153, v147
	v_pk_mul_f32 v[150:151], v[14:15], v[146:147] op_sel_hi:[1,0]
	v_fmac_f32_e32 v219, 0x3c000000, v147
	v_pk_mul_f32 v[150:151], v[198:199], v[150:151]
	v_rsq_f32_e32 v148, v219
	s_waitcnt vmcnt(3)
	v_pk_mul_f32 v[152:153], v[142:143], v[150:151]
	v_pk_mul_f32 v[150:151], v[144:145], v[150:151]
	v_add_f32_e32 v147, v152, v153
	v_add_f32_e32 v149, v150, v151
	v_pk_mul_f32 v[150:151], v[16:17], v[146:147] op_sel_hi:[1,0]
	v_ashrrev_i32_e32 v171, 31, v170
	v_pk_mul_f32 v[150:151], v[200:201], v[150:151]
	v_or_b32_e32 v172, s0, v212
	s_waitcnt vmcnt(2)
	v_pk_mul_f32 v[152:153], v[138:139], v[150:151]
	v_pk_mul_f32 v[150:151], v[140:141], v[150:151]
	v_add_f32_e32 v152, v152, v153
	v_add_f32_e32 v151, v150, v151
	v_cvt_pk_f16_f32 v150, v147, v149
	v_cvt_pk_f16_f32 v151, v152, v151
	ds_write_b64 v154, v[150:151] offset:25344
	v_pk_mul_f32 v[150:151], v[10:11], v[148:149] op_sel_hi:[1,0]
	v_ashrrev_i32_e32 v173, 31, v172
	v_pk_mul_f32 v[150:151], v[198:199], v[150:151]
	v_or_b32_e32 v174, s0, v203
	v_pk_mul_f32 v[142:143], v[142:143], v[150:151]
	v_ashrrev_i32_e32 v175, 31, v174
	v_add_f32_e32 v147, v142, v143
	v_pk_mul_f32 v[142:143], v[144:145], v[150:151]
	v_or_b32_e32 v176, s0, v208
	v_add_f32_e32 v144, v142, v143
	v_pk_mul_f32 v[142:143], v[12:13], v[148:149] op_sel_hi:[1,0]
	v_ashrrev_i32_e32 v177, 31, v176
	v_pk_mul_f32 v[142:143], v[200:201], v[142:143]
	v_or_b32_e32 v178, s0, v209
	v_pk_mul_f32 v[138:139], v[138:139], v[142:143]
	v_ashrrev_i32_e32 v179, 31, v178
	v_add_f32_e32 v145, v138, v139
	v_pk_mul_f32 v[138:139], v[140:141], v[142:143]
	v_or_b32_e32 v180, s0, v210
	v_add_f32_e32 v139, v138, v139
	v_cvt_pk_f16_f32 v138, v147, v144
	v_cvt_pk_f16_f32 v139, v145, v139
	ds_write_b64 v154, v[138:139] offset:25600
	v_pk_mul_f32 v[138:139], v[2:3], v[146:147] op_sel_hi:[1,0]
	v_ashrrev_i32_e32 v181, 31, v180
	v_pk_mul_f32 v[138:139], v[194:195], v[138:139]
	s_waitcnt vmcnt(1)
	v_pk_mul_f32 v[140:141], v[134:135], v[138:139]
	v_pk_mul_f32 v[138:139], v[136:137], v[138:139]
	v_add_f32_e32 v142, v140, v141
	v_add_f32_e32 v143, v138, v139
	v_pk_mul_f32 v[138:139], v[4:5], v[146:147] op_sel_hi:[1,0]
	s_nop 0
	v_pk_mul_f32 v[138:139], v[196:197], v[138:139]
	s_waitcnt vmcnt(0)
	v_pk_mul_f32 v[140:141], v[130:131], v[138:139]
	v_pk_mul_f32 v[138:139], v[132:133], v[138:139]
	v_add_f32_e32 v140, v140, v141
	v_add_f32_e32 v139, v138, v139
	v_cvt_pk_f16_f32 v138, v142, v143
	v_cvt_pk_f16_f32 v139, v140, v139
	ds_write_b64 v154, v[138:139] offset:25376
	v_pk_mul_f32 v[138:139], v[6:7], v[148:149] op_sel_hi:[1,0]
	s_nop 0
	v_pk_mul_f32 v[138:139], v[194:195], v[138:139]
	s_nop 0
	v_pk_mul_f32 v[134:135], v[134:135], v[138:139]
	s_nop 0
	v_add_f32_e32 v140, v134, v135
	v_pk_mul_f32 v[134:135], v[136:137], v[138:139]
	s_nop 0
	v_add_f32_e32 v136, v134, v135
	v_pk_mul_f32 v[134:135], v[8:9], v[148:149] op_sel_hi:[1,0]
	s_nop 0
	v_pk_mul_f32 v[134:135], v[196:197], v[134:135]
	s_nop 0
	v_pk_mul_f32 v[130:131], v[130:131], v[134:135]
	s_nop 0
	v_add_f32_e32 v137, v130, v131
	v_pk_mul_f32 v[130:131], v[132:133], v[134:135]
	v_lshlrev_b64 v[134:135], 8, v[168:169]
	v_add_f32_e32 v131, v130, v131
	v_cvt_pk_f16_f32 v130, v140, v136
	v_cvt_pk_f16_f32 v131, v137, v131
	ds_write_b64 v154, v[130:131] offset:25632
	v_mul_u32_u24_e32 v130, 0x210, v213
	v_add3_u32 v144, 0, v130, v202
	s_waitcnt lgkmcnt(0)
	s_barrier
	ds_read_b128 v[130:133], v144
	v_lshl_add_u64 v[138:139], v[166:167], 0, v[134:135]
	ds_read_b128 v[134:137], v144 offset:256
	v_add_u32_e32 v152, 0x8400, v144
	v_add_u32_e32 v160, 0x8400, v152
	s_waitcnt lgkmcnt(1)
	global_store_dwordx4 v[138:139], v[130:133], off sc0 sc1
	v_lshlrev_b64 v[138:139], 8, v[170:171]
	v_lshl_add_u64 v[142:143], v[166:167], 0, v[138:139]
	v_mul_u32_u24_e32 v130, 0x210, v211
	v_add3_u32 v140, 0, v130, v202
	ds_read_b128 v[130:133], v140
	ds_read_b128 v[138:141], v140 offset:256
	s_waitcnt lgkmcnt(1)
	global_store_dwordx4 v[142:143], v[130:133], off sc0 sc1
	ds_read_b128 v[130:133], v144 offset:33792
	v_lshlrev_b64 v[142:143], 8, v[172:173]
	v_lshl_add_u64 v[146:147], v[166:167], 0, v[142:143]
	ds_read_b128 v[142:145], v144 offset:34048
	s_waitcnt lgkmcnt(1)
	global_store_dwordx4 v[146:147], v[130:133], off sc0 sc1
	v_lshlrev_b64 v[146:147], 8, v[174:175]
	s_nop 0
	v_mul_u32_u24_e32 v130, 0x210, v203
	v_add3_u32 v148, 0, v130, v202
	ds_read_b128 v[130:133], v148
	v_lshl_add_u64 v[150:151], v[166:167], 0, v[146:147]
	ds_read_b128 v[146:149], v148 offset:256
	s_waitcnt lgkmcnt(1)
	global_store_dwordx4 v[150:151], v[130:133], off sc0 sc1
	ds_read_b128 v[130:133], v152 offset:33792
	v_lshlrev_b64 v[150:151], 8, v[176:177]
	v_lshl_add_u64 v[154:155], v[166:167], 0, v[150:151]
	ds_read_b128 v[150:153], v152 offset:34048
	s_waitcnt lgkmcnt(1)
	global_store_dwordx4 v[154:155], v[130:133], off sc0 sc1
	v_lshlrev_b64 v[154:155], 8, v[178:179]
	s_nop 0
	v_mul_u32_u24_e32 v130, 0x210, v209
	v_add3_u32 v156, 0, v130, v202
	ds_read_b128 v[130:133], v156
	v_lshl_add_u64 v[158:159], v[166:167], 0, v[154:155]
	ds_read_b128 v[154:157], v156 offset:256
	s_waitcnt lgkmcnt(1)
	global_store_dwordx4 v[158:159], v[130:133], off sc0 sc1
	ds_read_b128 v[130:133], v160 offset:33792
	v_lshlrev_b64 v[158:159], 8, v[180:181]
	v_lshl_add_u64 v[162:163], v[166:167], 0, v[158:159]
	ds_read_b128 v[158:161], v160 offset:34048
	s_waitcnt lgkmcnt(1)
	global_store_dwordx4 v[162:163], v[130:133], off sc0 sc1
	v_or_b32_e32 v162, s0, v1
	s_nop 0
	v_mul_u32_u24_e32 v130, 0x210, v1
	v_add3_u32 v130, 0, v130, v202
	ds_read_b128 v[130:133], v130
	v_ashrrev_i32_e32 v163, 31, v162
	v_lshlrev_b64 v[162:163], 8, v[162:163]
	v_lshl_add_u64 v[182:183], v[166:167], 0, v[162:163]
	v_or_b32_e32 v1, 0xe00, v0
	s_waitcnt lgkmcnt(0)
	global_store_dwordx4 v[182:183], v[130:133], off sc0 sc1
	v_lshrrev_b32_e32 v1, 4, v1
	v_mul_u32_u24_e32 v162, 0x210, v1
	v_or_b32_e32 v130, 0x800, v168
	v_ashrrev_i32_e32 v131, 31, v130
	v_lshlrev_b64 v[130:131], 8, v[130:131]
	v_lshl_add_u64 v[130:131], v[166:167], 0, v[130:131]
	global_store_dwordx4 v[130:131], v[134:137], off sc0 sc1
	v_or_b32_e32 v130, 0x800, v170
	v_ashrrev_i32_e32 v131, 31, v130
	v_lshlrev_b64 v[130:131], 8, v[130:131]
	v_lshl_add_u64 v[130:131], v[166:167], 0, v[130:131]
	global_store_dwordx4 v[130:131], v[138:141], off sc0 sc1
	v_or_b32_e32 v130, 0x800, v172
	v_ashrrev_i32_e32 v131, 31, v130
	v_lshlrev_b64 v[130:131], 8, v[130:131]
	v_lshl_add_u64 v[130:131], v[166:167], 0, v[130:131]
	global_store_dwordx4 v[130:131], v[142:145], off sc0 sc1
	v_or_b32_e32 v130, 0x800, v174
	v_ashrrev_i32_e32 v131, 31, v130
	v_lshlrev_b64 v[130:131], 8, v[130:131]
	v_lshl_add_u64 v[130:131], v[166:167], 0, v[130:131]
	global_store_dwordx4 v[130:131], v[146:149], off sc0 sc1
	v_or_b32_e32 v130, 0x800, v176
	v_ashrrev_i32_e32 v131, 31, v130
	v_lshlrev_b64 v[130:131], 8, v[130:131]
	v_lshl_add_u64 v[130:131], v[166:167], 0, v[130:131]
	global_store_dwordx4 v[130:131], v[150:153], off sc0 sc1
	v_or_b32_e32 v130, 0x800, v178
	v_ashrrev_i32_e32 v131, 31, v130
	v_lshlrev_b64 v[130:131], 8, v[130:131]
	v_lshl_add_u64 v[130:131], v[166:167], 0, v[130:131]
	global_store_dwordx4 v[130:131], v[154:157], off sc0 sc1
	v_or_b32_e32 v130, 0x800, v180
	v_ashrrev_i32_e32 v131, 31, v130
	v_add3_u32 v162, 0, v162, v202
	v_lshlrev_b64 v[130:131], 8, v[130:131]
	ds_read_b128 v[162:165], v162 offset:256
	v_lshl_add_u64 v[130:131], v[166:167], 0, v[130:131]
	s_addk_i32 s0, 0x800
	global_store_dwordx4 v[130:131], v[158:161], off sc0 sc1
	v_or_b32_e32 v130, s0, v1
	v_ashrrev_i32_e32 v131, 31, v130
	v_lshlrev_b64 v[130:131], 8, v[130:131]
	v_lshl_add_u64 v[130:131], v[166:167], 0, v[130:131]
	s_mov_b64 s[0:1], 0
	s_waitcnt lgkmcnt(0)
	global_store_dwordx4 v[130:131], v[162:165], off sc0 sc1

.LBB1_70:
	s_or_b64 exec, exec, s[26:27]
	s_lshr_b32 s2, s2, 7
	s_and_b32 s23, s2, 14
	s_and_b32 s2, s39, -8
	v_or_b32_e32 v231, v214, v1
	v_lshrrev_b32_e32 v228, 4, v0
	v_bfe_u32 v230, v0, 4, 2
	s_cmp_lg_u32 s2, 16
	s_mov_b64 s[2:3], -1
	s_cbranch_scc0 .LBB1_104
	v_lshlrev_b32_e32 v130, 2, v230
	s_and_b32 s25, s22, 0x700
	v_lshl_or_b32 v215, v226, 5, v130
	v_or_b32_e32 v130, s25, v231
	v_lshrrev_b32_e32 v131, 1, v215
	v_lshlrev_b32_e32 v130, 6, v130
	v_or_b32_e32 v132, v130, v131
	v_lshlrev_b32_e32 v132, 4, v132
	global_load_dwordx4 v[186:189], v132, s[16:17] offset:16
	global_load_dwordx4 v[190:193], v132, s[16:17]
	v_or_b32_e32 v132, 8, v131
	v_or_b32_e32 v133, v130, v132
	v_lshlrev_b32_e32 v133, 4, v133
	global_load_dwordx4 v[178:181], v133, s[16:17] offset:16
	global_load_dwordx4 v[182:185], v133, s[16:17]
	v_or_b32_e32 v133, 0x400, v130
	v_or_b32_e32 v134, v133, v131
	v_or_b32_e32 v133, v133, v132
	v_lshlrev_b32_e32 v134, 4, v134
	v_lshlrev_b32_e32 v133, 4, v133
	global_load_dwordx4 v[170:173], v134, s[16:17] offset:16
	global_load_dwordx4 v[174:177], v134, s[16:17]
	global_load_dwordx4 v[162:165], v133, s[16:17] offset:16
	global_load_dwordx4 v[166:169], v133, s[16:17]
	v_or_b32_e32 v133, 0x800, v130
	s_cmp_lt_u32 s39, 8
	v_or_b32_e32 v134, v133, v131
	v_or_b32_e32 v130, 0xc00, v130
	s_cselect_b64 vcc, -1, 0
	v_lshlrev_b32_e32 v134, 4, v134
	v_or_b32_e32 v133, v133, v132
	v_or_b32_e32 v131, v130, v131
	v_or_b32_e32 v130, v130, v132
	s_and_b64 s[2:3], vcc, exec
	global_load_dwordx4 v[154:157], v134, s[16:17] offset:16
	global_load_dwordx4 v[158:161], v134, s[16:17]
	v_lshlrev_b32_e32 v133, 4, v133
	v_lshlrev_b32_e32 v131, 4, v131
	v_lshlrev_b32_e32 v134, 4, v130
	s_cselect_b32 s3, s19, s5
	s_cselect_b32 s2, s18, s4
	v_lshlrev_b32_e32 v194, 2, v215
	global_load_dwordx4 v[146:149], v133, s[16:17] offset:16
	global_load_dwordx4 v[150:153], v133, s[16:17]
	global_load_dwordx4 v[138:141], v131, s[16:17] offset:16
	global_load_dwordx4 v[142:145], v131, s[16:17]
	s_nop 0
	global_load_dwordx4 v[130:133], v134, s[16:17] offset:16
	s_nop 0
	global_load_dwordx4 v[134:137], v134, s[16:17]
	s_nop 0
	global_load_dwordx4 v[198:201], v194, s[2:3]
	s_nop 0
	global_load_dwordx4 v[194:197], v194, s[2:3] offset:64
	v_fma_f32 v213, v122, v122, 0
	v_fmac_f32_e32 v213, v123, v123
	v_fmac_f32_e32 v213, v124, v124
	v_fmac_f32_e32 v213, v125, v125
	v_fmac_f32_e32 v213, v114, v114
	v_fmac_f32_e32 v213, v115, v115
	v_fmac_f32_e32 v213, v116, v116
	v_fmac_f32_e32 v213, v117, v117
	v_mov_b32_e32 v229, v213
	s_nop 1
	v_permlane16_swap_b32_e32 v213, v229
	s_add_i32 s4, 0, 0x21000
	v_add_f32_e32 v232, v213, v229
	v_lshl_add_u32 v212, v226, 2, s4
	v_mov_b32_e32 v233, v232
	v_cmp_eq_u32_e64 s[2:3], 0, v230
	s_nop 0
	v_permlane32_swap_b32_e32 v232, v233
	v_lshl_add_u32 v213, v231, 4, v212
	s_barrier
	s_and_saveexec_b64 s[4:5], s[2:3]
	v_add_f32_e32 v229, v232, v233
	ds_write_b32 v213, v229
	s_or_b64 exec, exec, s[4:5]
	v_fma_f32 v229, v102, v102, 0
	v_fmac_f32_e32 v229, v103, v103
	v_fmac_f32_e32 v229, v104, v104
	v_fmac_f32_e32 v229, v105, v105
	v_fmac_f32_e32 v229, v98, v98
	v_fmac_f32_e32 v229, v99, v99
	v_fmac_f32_e32 v229, v100, v100
	v_fmac_f32_e32 v229, v101, v101
	v_mov_b32_e32 v232, v229
	s_nop 1
	v_permlane16_swap_b32_e32 v229, v232
	v_add_f32_e32 v232, v229, v232
	v_mov_b32_e32 v233, v232
	s_nop 1
	v_permlane32_swap_b32_e32 v232, v233
	s_and_saveexec_b64 s[4:5], s[2:3]
	v_add_f32_e32 v229, v232, v233
	ds_write_b32 v213, v229 offset:256
	s_or_b64 exec, exec, s[4:5]
	v_fma_f32 v229, v86, v86, 0
	v_fmac_f32_e32 v229, v87, v87
	v_fmac_f32_e32 v229, v88, v88
	v_fmac_f32_e32 v229, v89, v89
	v_fmac_f32_e32 v229, v82, v82
	v_fmac_f32_e32 v229, v83, v83
	v_fmac_f32_e32 v229, v84, v84
	v_fmac_f32_e32 v229, v85, v85
	v_mov_b32_e32 v232, v229
	s_nop 1
	v_permlane16_swap_b32_e32 v229, v232
	v_add_f32_e32 v232, v229, v232
	v_mov_b32_e32 v233, v232
	s_nop 1
	v_permlane32_swap_b32_e32 v232, v233
	s_and_saveexec_b64 s[4:5], s[2:3]
	v_add_f32_e32 v229, v232, v233
	ds_write_b32 v213, v229 offset:512
	s_or_b64 exec, exec, s[4:5]
	v_fma_f32 v229, v70, v70, 0
	v_fmac_f32_e32 v229, v71, v71
	v_fmac_f32_e32 v229, v72, v72
	v_fmac_f32_e32 v229, v73, v73
	v_fmac_f32_e32 v229, v58, v58
	v_fmac_f32_e32 v229, v59, v59
	v_fmac_f32_e32 v229, v60, v60
	v_fmac_f32_e32 v229, v61, v61
	v_mov_b32_e32 v232, v229
	s_nop 1
	v_permlane16_swap_b32_e32 v229, v232
	v_add_f32_e32 v232, v229, v232
	v_mov_b32_e32 v233, v232
	s_nop 1
	v_permlane32_swap_b32_e32 v232, v233
	s_and_saveexec_b64 s[4:5], s[2:3]
	v_add_f32_e32 v229, v232, v233
	ds_write_b32 v213, v229 offset:768
	s_or_b64 exec, exec, s[4:5]
	v_fma_f32 v229, v66, v66, 0
	v_fmac_f32_e32 v229, v67, v67
	v_fmac_f32_e32 v229, v68, v68
	v_fmac_f32_e32 v229, v69, v69
	v_fmac_f32_e32 v229, v50, v50
	v_fmac_f32_e32 v229, v51, v51
	v_fmac_f32_e32 v229, v52, v52
	v_fmac_f32_e32 v229, v53, v53
	v_mov_b32_e32 v232, v229
	s_nop 1
	v_permlane16_swap_b32_e32 v229, v232
	v_add_f32_e32 v232, v229, v232
	v_mov_b32_e32 v233, v232
	s_nop 1
	v_permlane32_swap_b32_e32 v232, v233
	s_and_saveexec_b64 s[4:5], s[2:3]
	v_add_f32_e32 v229, v232, v233
	ds_write_b32 v213, v229 offset:2048
	s_or_b64 exec, exec, s[4:5]
	v_fma_f32 v229, v46, v46, 0
	v_fmac_f32_e32 v229, v47, v47
	v_fmac_f32_e32 v229, v48, v48
	v_fmac_f32_e32 v229, v49, v49
	v_fmac_f32_e32 v229, v34, v34
	v_fmac_f32_e32 v229, v35, v35
	v_fmac_f32_e32 v229, v36, v36
	v_fmac_f32_e32 v229, v37, v37
	v_mov_b32_e32 v232, v229
	s_nop 1
	v_permlane16_swap_b32_e32 v229, v232
	v_add_f32_e32 v232, v229, v232
	v_mov_b32_e32 v233, v232
	s_nop 1
	v_permlane32_swap_b32_e32 v232, v233
	s_and_saveexec_b64 s[4:5], s[2:3]
	v_add_f32_e32 v229, v232, v233
	ds_write_b32 v213, v229 offset:2304
	s_or_b64 exec, exec, s[4:5]
	v_fma_f32 v229, v30, v30, 0
	v_fmac_f32_e32 v229, v31, v31
	v_fmac_f32_e32 v229, v32, v32
	v_fmac_f32_e32 v229, v33, v33
	v_fmac_f32_e32 v229, v18, v18
	v_fmac_f32_e32 v229, v19, v19
	v_fmac_f32_e32 v229, v20, v20
	v_fmac_f32_e32 v229, v21, v21
	v_mov_b32_e32 v232, v229
	s_nop 1
	v_permlane16_swap_b32_e32 v229, v232
	v_add_f32_e32 v232, v229, v232
	v_mov_b32_e32 v233, v232
	s_nop 1
	v_permlane32_swap_b32_e32 v232, v233
	s_and_saveexec_b64 s[4:5], s[2:3]
	v_add_f32_e32 v229, v232, v233
	ds_write_b32 v213, v229 offset:2560
	s_or_b64 exec, exec, s[4:5]
	v_fma_f32 v229, v14, v14, 0
	v_fmac_f32_e32 v229, v15, v15
	v_fmac_f32_e32 v229, v16, v16
	v_fmac_f32_e32 v229, v17, v17
	v_fmac_f32_e32 v229, v2, v2
	v_fmac_f32_e32 v229, v3, v3
	v_fmac_f32_e32 v229, v4, v4
	v_fmac_f32_e32 v229, v5, v5
	v_mov_b32_e32 v232, v229
	s_nop 1
	v_permlane16_swap_b32_e32 v229, v232
	v_add_f32_e32 v232, v229, v232
	v_mov_b32_e32 v233, v232
	s_nop 1
	v_permlane32_swap_b32_e32 v232, v233
	s_and_saveexec_b64 s[4:5], s[2:3]
	v_add_f32_e32 v229, v232, v233
	ds_write_b32 v213, v229 offset:2816
	s_or_b64 exec, exec, s[4:5]
	v_fma_f32 v213, v126, v126, 0
	v_fmac_f32_e32 v213, v127, v127
	v_fmac_f32_e32 v213, v128, v128
	v_fmac_f32_e32 v213, v129, v129
	v_fmac_f32_e32 v213, v118, v118
	v_fmac_f32_e32 v213, v119, v119
	v_fmac_f32_e32 v213, v120, v120
	v_fmac_f32_e32 v213, v121, v121
	v_mov_b32_e32 v232, v213
	s_nop 1
	v_permlane16_swap_b32_e32 v213, v232
	v_add_f32_e32 v213, v213, v232
	v_or_b32_e32 v229, 0x100, v231
	v_mov_b32_e32 v232, v213
	s_nop 1
	v_permlane32_swap_b32_e32 v213, v232
	v_lshl_add_u32 v212, v229, 4, v212
	s_and_saveexec_b64 s[4:5], s[2:3]
	v_add_f32_e32 v213, v213, v232
	ds_write_b32 v212, v213
	s_or_b64 exec, exec, s[4:5]
	v_fma_f32 v213, v110, v110, 0
	v_fmac_f32_e32 v213, v111, v111
	v_fmac_f32_e32 v213, v112, v112
	v_fmac_f32_e32 v213, v113, v113
	v_fmac_f32_e32 v213, v106, v106
	v_fmac_f32_e32 v213, v107, v107
	v_fmac_f32_e32 v213, v108, v108
	v_fmac_f32_e32 v213, v109, v109
	v_mov_b32_e32 v229, v213
	s_nop 1
	v_permlane16_swap_b32_e32 v213, v229
	v_add_f32_e32 v213, v213, v229
	v_mov_b32_e32 v232, v213
	s_nop 1
	v_permlane32_swap_b32_e32 v213, v232
	s_and_saveexec_b64 s[4:5], s[2:3]
	v_add_f32_e32 v213, v213, v232
	ds_write_b32 v212, v213 offset:256
	s_or_b64 exec, exec, s[4:5]
	v_fma_f32 v213, v94, v94, 0
	v_fmac_f32_e32 v213, v95, v95
	v_fmac_f32_e32 v213, v96, v96
	v_fmac_f32_e32 v213, v97, v97
	v_fmac_f32_e32 v213, v90, v90
	v_fmac_f32_e32 v213, v91, v91
	v_fmac_f32_e32 v213, v92, v92
	v_fmac_f32_e32 v213, v93, v93
	v_mov_b32_e32 v229, v213
	s_nop 1
	v_permlane16_swap_b32_e32 v213, v229
	v_add_f32_e32 v213, v213, v229
	v_mov_b32_e32 v232, v213
	s_nop 1
	v_permlane32_swap_b32_e32 v213, v232
	s_and_saveexec_b64 s[4:5], s[2:3]
	v_add_f32_e32 v213, v213, v232
	ds_write_b32 v212, v213 offset:512
	s_or_b64 exec, exec, s[4:5]
	v_fma_f32 v213, v78, v78, 0
	v_fmac_f32_e32 v213, v79, v79
	v_fmac_f32_e32 v213, v80, v80
	v_fmac_f32_e32 v213, v81, v81
	v_fmac_f32_e32 v213, v74, v74
	v_fmac_f32_e32 v213, v75, v75
	v_fmac_f32_e32 v213, v76, v76
	v_fmac_f32_e32 v213, v77, v77
	v_mov_b32_e32 v229, v213
	s_nop 1
	v_permlane16_swap_b32_e32 v213, v229
	v_add_f32_e32 v213, v213, v229
	v_mov_b32_e32 v232, v213
	s_nop 1
	v_permlane32_swap_b32_e32 v213, v232
	s_and_saveexec_b64 s[4:5], s[2:3]
	v_add_f32_e32 v213, v213, v232
	ds_write_b32 v212, v213 offset:768
	s_or_b64 exec, exec, s[4:5]
	v_fma_f32 v213, v62, v62, 0
	v_fmac_f32_e32 v213, v63, v63
	v_fmac_f32_e32 v213, v64, v64
	v_fmac_f32_e32 v213, v65, v65
	v_fmac_f32_e32 v213, v54, v54
	v_fmac_f32_e32 v213, v55, v55
	v_fmac_f32_e32 v213, v56, v56
	v_fmac_f32_e32 v213, v57, v57
	v_mov_b32_e32 v229, v213
	s_nop 1
	v_permlane16_swap_b32_e32 v213, v229
	v_add_f32_e32 v213, v213, v229
	v_mov_b32_e32 v232, v213
	s_nop 1
	v_permlane32_swap_b32_e32 v213, v232
	s_and_saveexec_b64 s[4:5], s[2:3]
	v_add_f32_e32 v213, v213, v232
	ds_write_b32 v212, v213 offset:2048
	s_or_b64 exec, exec, s[4:5]
	v_fma_f32 v213, v42, v42, 0
	v_fmac_f32_e32 v213, v43, v43
	v_fmac_f32_e32 v213, v44, v44
	v_fmac_f32_e32 v213, v45, v45
	v_fmac_f32_e32 v213, v38, v38
	v_fmac_f32_e32 v213, v39, v39
	v_fmac_f32_e32 v213, v40, v40
	v_fmac_f32_e32 v213, v41, v41
	v_mov_b32_e32 v229, v213
	s_nop 1
	v_permlane16_swap_b32_e32 v213, v229
	v_add_f32_e32 v213, v213, v229
	v_mov_b32_e32 v232, v213
	s_nop 1
	v_permlane32_swap_b32_e32 v213, v232
	s_and_saveexec_b64 s[4:5], s[2:3]
	v_add_f32_e32 v213, v213, v232
	ds_write_b32 v212, v213 offset:2304
	s_or_b64 exec, exec, s[4:5]
	v_fma_f32 v213, v26, v26, 0
	v_fmac_f32_e32 v213, v27, v27
	v_fmac_f32_e32 v213, v28, v28
	v_fmac_f32_e32 v213, v29, v29
	v_fmac_f32_e32 v213, v22, v22
	v_fmac_f32_e32 v213, v23, v23
	v_fmac_f32_e32 v213, v24, v24
	v_fmac_f32_e32 v213, v25, v25
	v_mov_b32_e32 v229, v213
	s_nop 1
	v_permlane16_swap_b32_e32 v213, v229
	v_add_f32_e32 v213, v213, v229
	v_mov_b32_e32 v232, v213
	s_nop 1
	v_permlane32_swap_b32_e32 v213, v232
	s_and_saveexec_b64 s[4:5], s[2:3]
	v_add_f32_e32 v213, v213, v232
	ds_write_b32 v212, v213 offset:2560
	s_or_b64 exec, exec, s[4:5]
	v_fma_f32 v213, v10, v10, 0
	v_fmac_f32_e32 v213, v11, v11
	v_fmac_f32_e32 v213, v12, v12
	v_fmac_f32_e32 v213, v13, v13
	v_fmac_f32_e32 v213, v6, v6
	v_fmac_f32_e32 v213, v7, v7
	v_fmac_f32_e32 v213, v8, v8
	v_fmac_f32_e32 v213, v9, v9
	v_mov_b32_e32 v229, v213
	s_nop 1
	v_permlane16_swap_b32_e32 v213, v229
	v_add_f32_e32 v213, v213, v229
	v_mov_b32_e32 v232, v213
	s_nop 1
	v_permlane32_swap_b32_e32 v213, v232
	s_and_saveexec_b64 s[4:5], s[2:3]
	v_add_f32_e32 v213, v213, v232
	ds_write_b32 v212, v213 offset:2816
	s_or_b64 exec, exec, s[4:5]
	v_mov_b32_e32 v212, 0x3e0293ee
	v_cndmask_b32_e32 v238, 1.0, v212, vcc
	s_waitcnt vmcnt(0)
	v_pk_mul_f32 v[212:213], v[238:239], v[198:199] op_sel_hi:[0,1]
	v_lshl_add_u32 v198, v231, 4, 0
	v_add_u32_e32 v232, 0x21000, v198
	s_waitcnt lgkmcnt(0)
	s_barrier
	ds_read_b128 v[234:237], v232
	v_pk_mul_f32 v[200:201], v[238:239], v[200:201] op_sel_hi:[0,1]
	v_pk_mul_f32 v[196:197], v[238:239], v[196:197] op_sel_hi:[0,1]
	v_pk_mul_f32 v[198:199], v[238:239], v[194:195] op_sel_hi:[0,1]
	ds_read_b128 v[238:241], v232 offset:4096
	s_waitcnt lgkmcnt(1)
	v_add_f32_e32 v195, v234, v235
	v_add_f32_e32 v195, v236, v195
	v_add_f32_e32 v195, v237, v195
	v_mov_b32_e32 v233, 0x322bcc77
	v_fmamk_f32 v195, v195, 0x3c000000, v233
	v_add_u32_e32 v194, s24, v214
	v_rsq_f32_e32 v214, v195
	s_waitcnt lgkmcnt(0)
	v_add_f32_e32 v195, v238, v239
	v_add_f32_e32 v195, v240, v195
	v_add_f32_e32 v195, v241, v195
	v_fmamk_f32 v195, v195, 0x3c000000, v233
	s_movk_i32 s2, 0x7c0
	v_rsq_f32_e32 v236, v195
	v_and_or_b32 v238, v194, s2, v1
	v_pk_mul_f32 v[194:195], v[122:123], v[214:215] op_sel_hi:[1,0]
	v_lshlrev_b32_e32 v229, 1, v215
	v_pk_mul_f32 v[194:195], v[212:213], v[194:195]
	v_mul_u32_u24_e32 v237, 0x210, v231
	v_pk_mul_f32 v[234:235], v[190:191], v[194:195]
	v_pk_mul_f32 v[194:195], v[192:193], v[194:195]
	v_add_f32_e32 v239, v234, v235
	v_add_f32_e32 v240, v194, v195
	v_pk_mul_f32 v[194:195], v[124:125], v[214:215] op_sel_hi:[1,0]
	s_mov_b64 s[2:3], 0x4000
	v_pk_mul_f32 v[194:195], v[200:201], v[194:195]
	s_nop 0
	v_pk_mul_f32 v[234:235], v[186:187], v[194:195]
	v_pk_mul_f32 v[194:195], v[188:189], v[194:195]
	v_add_f32_e32 v234, v234, v235
	v_add_f32_e32 v195, v194, v195
	v_cvt_pk_f16_f32 v194, v239, v240
	v_cvt_pk_f16_f32 v195, v234, v195
	v_add3_u32 v234, 0, v237, v229
	ds_write_b64 v234, v[194:195]
	v_pk_mul_f32 v[194:195], v[126:127], v[236:237] op_sel_hi:[1,0]
	s_nop 0
	v_pk_mul_f32 v[194:195], v[212:213], v[194:195]
	s_nop 0
	v_pk_mul_f32 v[190:191], v[190:191], v[194:195]
	s_nop 0
	v_add_f32_e32 v229, v190, v191
	v_pk_mul_f32 v[190:191], v[192:193], v[194:195]
	v_mov_b32_e32 v195, 0
	v_add_f32_e32 v192, v190, v191
	v_pk_mul_f32 v[190:191], v[128:129], v[236:237] op_sel_hi:[1,0]
	s_nop 0
	v_pk_mul_f32 v[190:191], v[200:201], v[190:191]
	s_nop 0
	v_pk_mul_f32 v[186:187], v[186:187], v[190:191]
	s_nop 0
	v_add_f32_e32 v193, v186, v187
	v_pk_mul_f32 v[186:187], v[188:189], v[190:191]
	s_nop 0
	v_add_f32_e32 v187, v186, v187
	v_cvt_pk_f16_f32 v186, v229, v192
	v_cvt_pk_f16_f32 v187, v193, v187
	ds_write_b64 v234, v[186:187] offset:256
	v_lshlrev_b32_e32 v186, 3, v215
	v_lshl_or_b32 v194, v238, 10, v186
	v_pk_mul_f32 v[238:239], v[114:115], v[214:215] op_sel_hi:[1,0]
	v_pk_mul_f32 v[214:215], v[116:117], v[214:215] op_sel_hi:[1,0]
	v_pk_mul_f32 v[238:239], v[198:199], v[238:239]
	v_pk_mul_f32 v[214:215], v[196:197], v[214:215]
	v_pk_mul_f32 v[240:241], v[182:183], v[238:239]
	v_pk_mul_f32 v[238:239], v[184:185], v[238:239]
	global_load_dwordx4 v[186:189], v194, s[16:17] offset:16
	global_load_dwordx4 v[190:193], v194, s[16:17]
	v_add_f32_e32 v235, v238, v239
	v_pk_mul_f32 v[238:239], v[178:179], v[214:215]
	v_pk_mul_f32 v[214:215], v[180:181], v[214:215]
	v_add_f32_e32 v229, v240, v241
	v_add_f32_e32 v215, v214, v215
	v_add_f32_e32 v237, v238, v239
	v_cvt_pk_f16_f32 v214, v229, v235
	v_cvt_pk_f16_f32 v215, v237, v215
	ds_write_b64 v234, v[214:215] offset:32
	v_pk_mul_f32 v[214:215], v[118:119], v[236:237] op_sel_hi:[1,0]
	s_nop 0
	v_pk_mul_f32 v[214:215], v[198:199], v[214:215]
	s_nop 0
	v_pk_mul_f32 v[182:183], v[182:183], v[214:215]
	s_nop 0
	v_add_f32_e32 v229, v182, v183
	v_pk_mul_f32 v[182:183], v[184:185], v[214:215]
	v_lshl_add_u64 v[214:215], s[16:17], 0, v[194:195]
	v_add_f32_e32 v184, v182, v183
	v_pk_mul_f32 v[182:183], v[120:121], v[236:237] op_sel_hi:[1,0]
	s_nop 0
	v_pk_mul_f32 v[182:183], v[196:197], v[182:183]
	s_nop 0
	v_pk_mul_f32 v[178:179], v[178:179], v[182:183]
	s_nop 0
	v_add_f32_e32 v185, v178, v179
	v_pk_mul_f32 v[178:179], v[180:181], v[182:183]
	s_nop 0
	v_add_f32_e32 v179, v178, v179
	v_cvt_pk_f16_f32 v178, v229, v184
	v_cvt_pk_f16_f32 v179, v185, v179
	ds_write_b64 v234, v[178:179] offset:288
	ds_read_b128 v[236:239], v232 offset:256
	global_load_dwordx4 v[178:181], v194, s[16:17] offset:144
	global_load_dwordx4 v[182:185], v194, s[16:17] offset:128
	ds_read_b128 v[240:243], v232 offset:4352
	s_waitcnt lgkmcnt(1)
	v_add_f32_e32 v194, v236, v237
	v_add_f32_e32 v194, v238, v194
	v_add_f32_e32 v194, v239, v194
	v_fmamk_f32 v194, v194, 0x3c000000, v233
	v_rsq_f32_e32 v236, v194
	s_waitcnt lgkmcnt(0)
	v_add_f32_e32 v194, v240, v241
	v_add_f32_e32 v194, v242, v194
	v_add_f32_e32 v194, v243, v194
	v_pk_mul_f32 v[240:241], v[102:103], v[236:237] op_sel_hi:[1,0]
	v_fmamk_f32 v194, v194, 0x3c000000, v233
	v_pk_mul_f32 v[240:241], v[212:213], v[240:241]
	v_rsq_f32_e32 v238, v194
	v_pk_mul_f32 v[242:243], v[174:175], v[240:241]
	v_pk_mul_f32 v[240:241], v[176:177], v[240:241]
	v_add_f32_e32 v194, v242, v243
	v_add_f32_e32 v229, v240, v241
	v_pk_mul_f32 v[240:241], v[104:105], v[236:237] op_sel_hi:[1,0]
	s_nop 0
	v_pk_mul_f32 v[240:241], v[200:201], v[240:241]
	s_nop 0
	v_pk_mul_f32 v[242:243], v[170:171], v[240:241]
	v_pk_mul_f32 v[240:241], v[172:173], v[240:241]
	v_add_f32_e32 v235, v242, v243
	v_add_f32_e32 v237, v240, v241
	v_cvt_pk_f16_f32 v240, v194, v229
	v_cvt_pk_f16_f32 v241, v235, v237
	ds_write_b64 v234, v[240:241] offset:8448
	v_pk_mul_f32 v[240:241], v[110:111], v[238:239] op_sel_hi:[1,0]
	v_pk_mul_f32 v[242:243], v[98:99], v[236:237] op_sel_hi:[1,0]
	v_pk_mul_f32 v[240:241], v[212:213], v[240:241]
	v_pk_mul_f32 v[242:243], v[198:199], v[242:243]
	v_pk_mul_f32 v[174:175], v[174:175], v[240:241]
	v_pk_mul_f32 v[236:237], v[100:101], v[236:237] op_sel_hi:[1,0]
	v_add_f32_e32 v229, v174, v175
	v_pk_mul_f32 v[174:175], v[176:177], v[240:241]
	v_pk_mul_f32 v[244:245], v[166:167], v[242:243]
	v_add_f32_e32 v176, v174, v175
	v_pk_mul_f32 v[174:175], v[112:113], v[238:239] op_sel_hi:[1,0]
	v_pk_mul_f32 v[242:243], v[168:169], v[242:243]
	v_pk_mul_f32 v[174:175], v[200:201], v[174:175]
	v_pk_mul_f32 v[236:237], v[196:197], v[236:237]
	v_pk_mul_f32 v[170:171], v[170:171], v[174:175]
	v_add_f32_e32 v235, v242, v243
	v_add_f32_e32 v177, v170, v171
	v_pk_mul_f32 v[170:171], v[172:173], v[174:175]
	v_pk_mul_f32 v[242:243], v[162:163], v[236:237]
	v_add_f32_e32 v171, v170, v171
	v_cvt_pk_f16_f32 v170, v229, v176
	v_cvt_pk_f16_f32 v171, v177, v171
	ds_write_b64 v234, v[170:171] offset:8704
	v_lshl_add_u64 v[170:171], v[214:215], 0, s[2:3]
	s_movk_i32 s2, 0x4000
	v_add_co_u32_e64 v240, s[2:3], s2, v214
	v_pk_mul_f32 v[236:237], v[164:165], v[236:237]
	s_nop 0
	v_addc_co_u32_e64 v241, s[2:3], 0, v215, s[2:3]
	v_add_f32_e32 v237, v236, v237
	global_load_dwordx4 v[174:177], v[240:241], off
	s_nop 0
	global_load_dwordx4 v[170:173], v[170:171], off offset:16
	v_add_f32_e32 v229, v244, v245
	v_add_f32_e32 v239, v242, v243
	v_cvt_pk_f16_f32 v236, v229, v235
	v_cvt_pk_f16_f32 v237, v239, v237
	ds_write_b64 v234, v[236:237] offset:8480
	v_pk_mul_f32 v[236:237], v[106:107], v[238:239] op_sel_hi:[1,0]
	s_mov_b64 s[2:3], 0x4080
	v_pk_mul_f32 v[236:237], v[198:199], v[236:237]
	v_add_u32_e32 v194, 0x2100, v234
	v_pk_mul_f32 v[166:167], v[166:167], v[236:237]
	s_nop 0
	v_add_f32_e32 v229, v166, v167
	v_pk_mul_f32 v[166:167], v[168:169], v[236:237]
	s_nop 0
	v_add_f32_e32 v168, v166, v167
	v_pk_mul_f32 v[166:167], v[108:109], v[238:239] op_sel_hi:[1,0]
	s_nop 0
	v_pk_mul_f32 v[166:167], v[196:197], v[166:167]
	s_nop 0
	v_pk_mul_f32 v[162:163], v[162:163], v[166:167]
	s_nop 0
	v_add_f32_e32 v169, v162, v163
	v_pk_mul_f32 v[162:163], v[164:165], v[166:167]
	s_nop 0
	v_add_f32_e32 v163, v162, v163
	v_cvt_pk_f16_f32 v162, v229, v168
	v_cvt_pk_f16_f32 v163, v169, v163
	ds_write_b64 v234, v[162:163] offset:8736
	ds_read_b128 v[236:239], v232 offset:512
	v_lshl_add_u64 v[162:163], v[214:215], 0, s[2:3]
	global_load_dwordx4 v[166:169], v[240:241], off offset:128
	s_nop 0
	global_load_dwordx4 v[162:165], v[162:163], off offset:16
	ds_read_b128 v[240:243], v232 offset:4608
	s_mov_b64 s[2:3], 0x8000
	s_waitcnt lgkmcnt(1)
	v_add_f32_e32 v229, v236, v237
	v_add_f32_e32 v229, v238, v229
	v_add_f32_e32 v229, v239, v229
	v_fmamk_f32 v229, v229, 0x3c000000, v233
	v_rsq_f32_e32 v236, v229
	s_waitcnt lgkmcnt(0)
	v_add_f32_e32 v229, v240, v241
	v_add_f32_e32 v229, v242, v229
	v_add_f32_e32 v229, v243, v229
	v_pk_mul_f32 v[240:241], v[86:87], v[236:237] op_sel_hi:[1,0]
	v_fmamk_f32 v229, v229, 0x3c000000, v233
	v_pk_mul_f32 v[240:241], v[212:213], v[240:241]
	v_rsq_f32_e32 v238, v229
	v_pk_mul_f32 v[242:243], v[158:159], v[240:241]
	v_pk_mul_f32 v[240:241], v[160:161], v[240:241]
	v_add_f32_e32 v229, v242, v243
	v_add_f32_e32 v235, v240, v241
	v_pk_mul_f32 v[240:241], v[88:89], v[236:237] op_sel_hi:[1,0]
	s_nop 0
	v_pk_mul_f32 v[240:241], v[200:201], v[240:241]
	s_nop 0
	v_pk_mul_f32 v[242:243], v[154:155], v[240:241]
	v_pk_mul_f32 v[240:241], v[156:157], v[240:241]
	v_add_f32_e32 v237, v242, v243
	v_add_f32_e32 v239, v240, v241
	v_cvt_pk_f16_f32 v240, v229, v235
	v_cvt_pk_f16_f32 v241, v237, v239
	ds_write_b64 v234, v[240:241] offset:16896
	v_pk_mul_f32 v[240:241], v[94:95], v[238:239] op_sel_hi:[1,0]
	v_pk_mul_f32 v[242:243], v[82:83], v[236:237] op_sel_hi:[1,0]
	v_pk_mul_f32 v[240:241], v[212:213], v[240:241]
	v_pk_mul_f32 v[242:243], v[198:199], v[242:243]
	v_pk_mul_f32 v[158:159], v[158:159], v[240:241]
	v_pk_mul_f32 v[236:237], v[84:85], v[236:237] op_sel_hi:[1,0]
	v_add_f32_e32 v229, v158, v159
	v_pk_mul_f32 v[158:159], v[160:161], v[240:241]
	v_pk_mul_f32 v[244:245], v[150:151], v[242:243]
	v_add_f32_e32 v160, v158, v159
	v_pk_mul_f32 v[158:159], v[96:97], v[238:239] op_sel_hi:[1,0]
	v_pk_mul_f32 v[242:243], v[152:153], v[242:243]
	v_pk_mul_f32 v[158:159], v[200:201], v[158:159]
	v_pk_mul_f32 v[236:237], v[196:197], v[236:237]
	v_pk_mul_f32 v[154:155], v[154:155], v[158:159]
	v_add_f32_e32 v235, v242, v243
	v_add_f32_e32 v161, v154, v155
	v_pk_mul_f32 v[154:155], v[156:157], v[158:159]
	v_pk_mul_f32 v[242:243], v[146:147], v[236:237]
	v_add_f32_e32 v155, v154, v155
	v_cvt_pk_f16_f32 v154, v229, v160
	v_cvt_pk_f16_f32 v155, v161, v155
	ds_write_b64 v234, v[154:155] offset:17152
	v_lshl_add_u64 v[154:155], v[214:215], 0, s[2:3]
	s_mov_b32 s2, 0x8000
	v_add_co_u32_e64 v240, s[2:3], s2, v214
	v_pk_mul_f32 v[236:237], v[148:149], v[236:237]
	s_nop 0
	v_addc_co_u32_e64 v241, s[2:3], 0, v215, s[2:3]
	v_add_f32_e32 v237, v236, v237
	global_load_dwordx4 v[158:161], v[240:241], off
	s_nop 0
	global_load_dwordx4 v[154:157], v[154:155], off offset:16
	v_add_f32_e32 v229, v244, v245
	v_add_f32_e32 v239, v242, v243
	v_cvt_pk_f16_f32 v236, v229, v235
	v_cvt_pk_f16_f32 v237, v239, v237
	ds_write_b64 v234, v[236:237] offset:16928
	v_pk_mul_f32 v[236:237], v[90:91], v[238:239] op_sel_hi:[1,0]
	s_mov_b64 s[2:3], 0x8080
	v_pk_mul_f32 v[236:237], v[198:199], v[236:237]
	s_nop 0
	v_pk_mul_f32 v[150:151], v[150:151], v[236:237]
	s_nop 0
	v_add_f32_e32 v229, v150, v151
	v_pk_mul_f32 v[150:151], v[152:153], v[236:237]
	s_nop 0
	v_add_f32_e32 v152, v150, v151
	v_pk_mul_f32 v[150:151], v[92:93], v[238:239] op_sel_hi:[1,0]
	s_nop 0
	v_pk_mul_f32 v[150:151], v[196:197], v[150:151]
	s_nop 0
	v_pk_mul_f32 v[146:147], v[146:147], v[150:151]
	s_nop 0
	v_add_f32_e32 v153, v146, v147
	v_pk_mul_f32 v[146:147], v[148:149], v[150:151]
	s_nop 0
	v_add_f32_e32 v147, v146, v147
	v_cvt_pk_f16_f32 v146, v229, v152
	v_cvt_pk_f16_f32 v147, v153, v147
	ds_write_b64 v234, v[146:147] offset:17184
	ds_read_b128 v[236:239], v232 offset:768
	v_lshl_add_u64 v[146:147], v[214:215], 0, s[2:3]
	global_load_dwordx4 v[150:153], v[240:241], off offset:128
	s_nop 0
	global_load_dwordx4 v[146:149], v[146:147], off offset:16
	ds_read_b128 v[240:243], v232 offset:4864
	s_mov_b64 s[2:3], 0xc000
	s_waitcnt lgkmcnt(1)
	v_add_f32_e32 v229, v236, v237
	v_add_f32_e32 v229, v238, v229
	v_add_f32_e32 v229, v239, v229
	v_fmamk_f32 v229, v229, 0x3c000000, v233
	v_rsq_f32_e32 v236, v229
	s_waitcnt lgkmcnt(0)
	v_add_f32_e32 v229, v240, v241
	v_add_f32_e32 v229, v242, v229
	v_add_f32_e32 v229, v243, v229
	v_pk_mul_f32 v[240:241], v[70:71], v[236:237] op_sel_hi:[1,0]
	v_fmamk_f32 v229, v229, 0x3c000000, v233
	v_pk_mul_f32 v[240:241], v[212:213], v[240:241]
	v_rsq_f32_e32 v238, v229
	v_pk_mul_f32 v[242:243], v[142:143], v[240:241]
	v_pk_mul_f32 v[240:241], v[144:145], v[240:241]
	v_add_f32_e32 v229, v242, v243
	v_add_f32_e32 v235, v240, v241
	v_pk_mul_f32 v[240:241], v[72:73], v[236:237] op_sel_hi:[1,0]
	s_nop 0
	v_pk_mul_f32 v[240:241], v[200:201], v[240:241]
	s_nop 0
	v_pk_mul_f32 v[242:243], v[138:139], v[240:241]
	v_pk_mul_f32 v[240:241], v[140:141], v[240:241]
	v_add_f32_e32 v237, v242, v243
	v_add_f32_e32 v239, v240, v241
	v_cvt_pk_f16_f32 v240, v229, v235
	v_cvt_pk_f16_f32 v241, v237, v239
	ds_write_b64 v234, v[240:241] offset:25344
	v_pk_mul_f32 v[240:241], v[78:79], v[238:239] op_sel_hi:[1,0]
	v_pk_mul_f32 v[242:243], v[58:59], v[236:237] op_sel_hi:[1,0]
	v_pk_mul_f32 v[240:241], v[212:213], v[240:241]
	v_pk_mul_f32 v[242:243], v[198:199], v[242:243]
	v_pk_mul_f32 v[142:143], v[142:143], v[240:241]
	v_pk_mul_f32 v[236:237], v[60:61], v[236:237] op_sel_hi:[1,0]
	v_add_f32_e32 v229, v142, v143
	v_pk_mul_f32 v[142:143], v[144:145], v[240:241]
	v_pk_mul_f32 v[244:245], v[134:135], v[242:243]
	v_add_f32_e32 v144, v142, v143
	v_pk_mul_f32 v[142:143], v[80:81], v[238:239] op_sel_hi:[1,0]
	v_pk_mul_f32 v[242:243], v[136:137], v[242:243]
	v_pk_mul_f32 v[142:143], v[200:201], v[142:143]
	v_pk_mul_f32 v[236:237], v[196:197], v[236:237]
	v_pk_mul_f32 v[138:139], v[138:139], v[142:143]
	v_add_f32_e32 v235, v242, v243
	v_add_f32_e32 v145, v138, v139
	v_pk_mul_f32 v[138:139], v[140:141], v[142:143]
	v_pk_mul_f32 v[242:243], v[130:131], v[236:237]
	v_add_f32_e32 v139, v138, v139
	v_cvt_pk_f16_f32 v138, v229, v144
	v_cvt_pk_f16_f32 v139, v145, v139
	ds_write_b64 v234, v[138:139] offset:25600
	v_lshl_add_u64 v[138:139], v[214:215], 0, s[2:3]
	s_mov_b32 s2, 0xc000
	v_add_co_u32_e64 v240, s[2:3], s2, v214
	v_pk_mul_f32 v[236:237], v[132:133], v[236:237]
	s_nop 0
	v_addc_co_u32_e64 v241, s[2:3], 0, v215, s[2:3]
	v_add_f32_e32 v237, v236, v237
	global_load_dwordx4 v[142:145], v[240:241], off
	s_nop 0
	global_load_dwordx4 v[138:141], v[138:139], off offset:16
	v_add_f32_e32 v229, v244, v245
	v_add_f32_e32 v239, v242, v243
	v_cvt_pk_f16_f32 v236, v229, v235
	v_cvt_pk_f16_f32 v237, v239, v237
	ds_write_b64 v234, v[236:237] offset:25376
	v_pk_mul_f32 v[236:237], v[74:75], v[238:239] op_sel_hi:[1,0]
	s_mov_b64 s[2:3], 0xc080
	v_pk_mul_f32 v[236:237], v[198:199], v[236:237]
	s_nop 0
	v_pk_mul_f32 v[134:135], v[134:135], v[236:237]
	s_nop 0
	v_add_f32_e32 v229, v134, v135
	v_pk_mul_f32 v[134:135], v[136:137], v[236:237]
	s_nop 0
	v_add_f32_e32 v136, v134, v135
	v_pk_mul_f32 v[134:135], v[76:77], v[238:239] op_sel_hi:[1,0]
	s_nop 0
	v_pk_mul_f32 v[134:135], v[196:197], v[134:135]
	s_nop 0
	v_pk_mul_f32 v[130:131], v[130:131], v[134:135]
	s_nop 0
	v_add_f32_e32 v137, v130, v131
	v_pk_mul_f32 v[130:131], v[132:133], v[134:135]
	s_nop 0
	v_add_f32_e32 v131, v130, v131
	v_cvt_pk_f16_f32 v130, v229, v136
	v_cvt_pk_f16_f32 v131, v137, v131
	ds_write_b64 v234, v[130:131] offset:25632
	ds_read_b128 v[236:239], v232 offset:2048
	v_lshl_add_u64 v[130:131], v[214:215], 0, s[2:3]
	global_load_dwordx4 v[134:137], v[240:241], off offset:128
	s_nop 0
	global_load_dwordx4 v[130:133], v[130:131], off offset:16
	ds_read_b128 v[240:243], v232 offset:6144
	s_and_b64 s[2:3], vcc, exec
	s_waitcnt lgkmcnt(1)
	v_add_f32_e32 v214, v236, v237
	v_add_f32_e32 v214, v238, v214
	v_add_f32_e32 v214, v239, v214
	v_fmamk_f32 v214, v214, 0x3c000000, v233
	v_rsq_f32_e32 v214, v214
	s_waitcnt lgkmcnt(0)
	v_add_f32_e32 v215, v240, v241
	v_add_f32_e32 v215, v242, v215
	v_add_f32_e32 v215, v243, v215
	v_fmamk_f32 v215, v215, 0x3c000000, v233
	v_pk_mul_f32 v[238:239], v[66:67], v[214:215] op_sel_hi:[1,0]
	v_rsq_f32_e32 v236, v215
	v_pk_mul_f32 v[238:239], v[212:213], v[238:239]
	s_cselect_b32 s3, s7, s9
	s_waitcnt vmcnt(14)
	v_pk_mul_f32 v[240:241], v[190:191], v[238:239]
	v_pk_mul_f32 v[238:239], v[192:193], v[238:239]
	v_add_f32_e32 v215, v240, v241
	v_add_f32_e32 v229, v238, v239
	v_pk_mul_f32 v[238:239], v[68:69], v[214:215] op_sel_hi:[1,0]
	s_cselect_b32 s2, s6, s8
	v_pk_mul_f32 v[238:239], v[200:201], v[238:239]
	s_lshl_b32 s4, s38, 1
	v_pk_mul_f32 v[240:241], v[186:187], v[238:239]
	v_pk_mul_f32 v[238:239], v[188:189], v[238:239]
	v_add_f32_e32 v235, v240, v241
	v_add_f32_e32 v237, v238, v239
	v_cvt_pk_f16_f32 v238, v215, v229
	v_cvt_pk_f16_f32 v239, v235, v237
	ds_write_b64 v194, v[238:239] offset:59136
	v_pk_mul_f32 v[238:239], v[62:63], v[236:237] op_sel_hi:[1,0]
	s_and_b32 s4, s4, 0x1ffff0
	v_pk_mul_f32 v[238:239], v[212:213], v[238:239]
	s_or_b32 s4, s4, s23
	v_pk_mul_f32 v[190:191], v[190:191], v[238:239]
	s_nop 0
	v_add_f32_e32 v215, v190, v191
	v_pk_mul_f32 v[190:191], v[192:193], v[238:239]
	s_nop 0
	v_add_f32_e32 v192, v190, v191
	v_pk_mul_f32 v[190:191], v[64:65], v[236:237] op_sel_hi:[1,0]
	s_nop 0
	v_pk_mul_f32 v[190:191], v[200:201], v[190:191]
	s_nop 0
	v_pk_mul_f32 v[186:187], v[186:187], v[190:191]
	s_nop 0
	v_add_f32_e32 v193, v186, v187
	v_pk_mul_f32 v[186:187], v[188:189], v[190:191]
	s_nop 0
	v_add_f32_e32 v187, v186, v187
	v_cvt_pk_f16_f32 v186, v215, v192
	v_cvt_pk_f16_f32 v187, v193, v187
	ds_write_b64 v194, v[186:187] offset:59392
	v_pk_mul_f32 v[186:187], v[50:51], v[214:215] op_sel_hi:[1,0]
	s_nop 0
	v_pk_mul_f32 v[186:187], v[198:199], v[186:187]
	s_waitcnt vmcnt(12)
	v_pk_mul_f32 v[188:189], v[182:183], v[186:187]
	v_pk_mul_f32 v[186:187], v[184:185], v[186:187]
	v_add_f32_e32 v190, v188, v189
	v_add_f32_e32 v191, v186, v187
	v_pk_mul_f32 v[186:187], v[52:53], v[214:215] op_sel_hi:[1,0]
	s_nop 0
	v_pk_mul_f32 v[186:187], v[196:197], v[186:187]
	s_nop 0
	v_pk_mul_f32 v[188:189], v[178:179], v[186:187]
	v_pk_mul_f32 v[186:187], v[180:181], v[186:187]
	v_add_f32_e32 v188, v188, v189
	v_add_f32_e32 v187, v186, v187
	v_cvt_pk_f16_f32 v186, v190, v191
	v_cvt_pk_f16_f32 v187, v188, v187
	ds_write_b64 v194, v[186:187] offset:59168
	v_pk_mul_f32 v[186:187], v[54:55], v[236:237] op_sel_hi:[1,0]
	s_nop 0
	v_pk_mul_f32 v[186:187], v[198:199], v[186:187]
	s_nop 0
	v_pk_mul_f32 v[182:183], v[182:183], v[186:187]
	s_nop 0
	v_add_f32_e32 v188, v182, v183
	v_pk_mul_f32 v[182:183], v[184:185], v[186:187]
	v_add_u32_e32 v186, 0x4200, v234
	v_add_f32_e32 v184, v182, v183
	v_pk_mul_f32 v[182:183], v[56:57], v[236:237] op_sel_hi:[1,0]
	s_nop 0
	v_pk_mul_f32 v[182:183], v[196:197], v[182:183]
	s_nop 0
	v_pk_mul_f32 v[178:179], v[178:179], v[182:183]
	s_nop 0
	v_add_f32_e32 v185, v178, v179
	v_pk_mul_f32 v[178:179], v[180:181], v[182:183]
	s_nop 0
	v_add_f32_e32 v179, v178, v179
	v_cvt_pk_f16_f32 v178, v188, v184
	v_cvt_pk_f16_f32 v179, v185, v179
	ds_write_b64 v194, v[178:179] offset:59424
	ds_read_b128 v[178:181], v232 offset:2304
	ds_read_b128 v[182:185], v232 offset:6400
	s_waitcnt lgkmcnt(1)
	v_add_f32_e32 v178, v178, v179
	v_add_f32_e32 v178, v180, v178
	v_add_f32_e32 v178, v181, v178
	v_fmamk_f32 v178, v178, 0x3c000000, v233
	v_rsq_f32_e32 v178, v178
	s_waitcnt lgkmcnt(0)
	v_add_f32_e32 v179, v182, v183
	v_add_f32_e32 v179, v184, v179
	v_add_f32_e32 v179, v185, v179
	v_fmamk_f32 v179, v179, 0x3c000000, v233
	v_pk_mul_f32 v[182:183], v[46:47], v[178:179] op_sel_hi:[1,0]
	v_rsq_f32_e32 v180, v179
	v_pk_mul_f32 v[182:183], v[212:213], v[182:183]
	s_waitcnt vmcnt(11)
	v_pk_mul_f32 v[184:185], v[174:175], v[182:183]
	v_pk_mul_f32 v[182:183], v[176:177], v[182:183]
	v_add_f32_e32 v179, v184, v185
	v_add_f32_e32 v181, v182, v183
	v_pk_mul_f32 v[182:183], v[48:49], v[178:179] op_sel_hi:[1,0]
	s_nop 0
	v_pk_mul_f32 v[182:183], v[200:201], v[182:183]
	s_waitcnt vmcnt(10)
	v_pk_mul_f32 v[184:185], v[170:171], v[182:183]
	v_pk_mul_f32 v[182:183], v[172:173], v[182:183]
	v_add_f32_e32 v184, v184, v185
	v_add_f32_e32 v183, v182, v183
	v_cvt_pk_f16_f32 v182, v179, v181
	v_cvt_pk_f16_f32 v183, v184, v183
	ds_write_b64 v186, v[182:183] offset:59136
	v_pk_mul_f32 v[182:183], v[42:43], v[180:181] op_sel_hi:[1,0]
	s_nop 0
	v_pk_mul_f32 v[182:183], v[212:213], v[182:183]
	s_nop 0
	v_pk_mul_f32 v[174:175], v[174:175], v[182:183]
	s_nop 0
	v_add_f32_e32 v179, v174, v175
	v_pk_mul_f32 v[174:175], v[176:177], v[182:183]
	s_nop 0
	v_add_f32_e32 v176, v174, v175
	v_pk_mul_f32 v[174:175], v[44:45], v[180:181] op_sel_hi:[1,0]
	s_nop 0
	v_pk_mul_f32 v[174:175], v[200:201], v[174:175]
	s_nop 0
	v_pk_mul_f32 v[170:171], v[170:171], v[174:175]
	s_nop 0
	v_add_f32_e32 v177, v170, v171
	v_pk_mul_f32 v[170:171], v[172:173], v[174:175]
	s_nop 0
	v_add_f32_e32 v171, v170, v171
	v_cvt_pk_f16_f32 v170, v179, v176
	v_cvt_pk_f16_f32 v171, v177, v171
	ds_write_b64 v186, v[170:171] offset:59392
	v_pk_mul_f32 v[170:171], v[34:35], v[178:179] op_sel_hi:[1,0]
	s_nop 0
	v_pk_mul_f32 v[170:171], v[198:199], v[170:171]
	s_waitcnt vmcnt(9)
	v_pk_mul_f32 v[172:173], v[166:167], v[170:171]
	v_pk_mul_f32 v[170:171], v[168:169], v[170:171]
	v_add_f32_e32 v174, v172, v173
	v_add_f32_e32 v175, v170, v171
	v_pk_mul_f32 v[170:171], v[36:37], v[178:179] op_sel_hi:[1,0]
	s_nop 0
	v_pk_mul_f32 v[170:171], v[196:197], v[170:171]
	s_waitcnt vmcnt(8)
	v_pk_mul_f32 v[172:173], v[162:163], v[170:171]
	v_pk_mul_f32 v[170:171], v[164:165], v[170:171]
	v_add_f32_e32 v172, v172, v173
	v_add_f32_e32 v171, v170, v171
	v_cvt_pk_f16_f32 v170, v174, v175
	v_cvt_pk_f16_f32 v171, v172, v171
	ds_write_b64 v186, v[170:171] offset:59168
	v_pk_mul_f32 v[170:171], v[38:39], v[180:181] op_sel_hi:[1,0]
	s_nop 0
	v_pk_mul_f32 v[170:171], v[198:199], v[170:171]
	s_nop 0
	v_pk_mul_f32 v[166:167], v[166:167], v[170:171]
	s_nop 0
	v_add_f32_e32 v172, v166, v167
	v_pk_mul_f32 v[166:167], v[168:169], v[170:171]
	v_add_u32_e32 v170, 0x6300, v234
	v_add_f32_e32 v168, v166, v167
	v_pk_mul_f32 v[166:167], v[40:41], v[180:181] op_sel_hi:[1,0]
	s_nop 0
	v_pk_mul_f32 v[166:167], v[196:197], v[166:167]
	s_nop 0
	v_pk_mul_f32 v[162:163], v[162:163], v[166:167]
	s_nop 0
	v_add_f32_e32 v169, v162, v163
	v_pk_mul_f32 v[162:163], v[164:165], v[166:167]
	s_nop 0
	v_add_f32_e32 v163, v162, v163
	v_cvt_pk_f16_f32 v162, v172, v168
	v_cvt_pk_f16_f32 v163, v169, v163
	ds_write_b64 v186, v[162:163] offset:59424
	ds_read_b128 v[162:165], v232 offset:2560
	ds_read_b128 v[166:169], v232 offset:6656
	s_waitcnt lgkmcnt(1)
	v_add_f32_e32 v162, v162, v163
	v_add_f32_e32 v162, v164, v162
	v_add_f32_e32 v162, v165, v162
	v_fmamk_f32 v162, v162, 0x3c000000, v233
	v_rsq_f32_e32 v162, v162
	s_waitcnt lgkmcnt(0)
	v_add_f32_e32 v163, v166, v167
	v_add_f32_e32 v163, v168, v163
	v_add_f32_e32 v163, v169, v163
	v_fmamk_f32 v163, v163, 0x3c000000, v233
	v_pk_mul_f32 v[166:167], v[30:31], v[162:163] op_sel_hi:[1,0]
	v_rsq_f32_e32 v164, v163
	v_pk_mul_f32 v[166:167], v[212:213], v[166:167]
	s_waitcnt vmcnt(7)
	v_pk_mul_f32 v[168:169], v[158:159], v[166:167]
	v_pk_mul_f32 v[166:167], v[160:161], v[166:167]
	v_add_f32_e32 v163, v168, v169
	v_add_f32_e32 v165, v166, v167
	v_pk_mul_f32 v[166:167], v[32:33], v[162:163] op_sel_hi:[1,0]
	s_nop 0
	v_pk_mul_f32 v[166:167], v[200:201], v[166:167]
	s_waitcnt vmcnt(6)
	v_pk_mul_f32 v[168:169], v[154:155], v[166:167]
	v_pk_mul_f32 v[166:167], v[156:157], v[166:167]
	v_add_f32_e32 v168, v168, v169
	v_add_f32_e32 v167, v166, v167
	v_cvt_pk_f16_f32 v166, v163, v165
	v_cvt_pk_f16_f32 v167, v168, v167
	ds_write_b64 v170, v[166:167] offset:59136
	v_pk_mul_f32 v[166:167], v[26:27], v[164:165] op_sel_hi:[1,0]
	s_nop 0
	v_pk_mul_f32 v[166:167], v[212:213], v[166:167]
	s_nop 0
	v_pk_mul_f32 v[158:159], v[158:159], v[166:167]
	s_nop 0
	v_add_f32_e32 v163, v158, v159
	v_pk_mul_f32 v[158:159], v[160:161], v[166:167]
	s_nop 0
	v_add_f32_e32 v160, v158, v159
	v_pk_mul_f32 v[158:159], v[28:29], v[164:165] op_sel_hi:[1,0]
	s_nop 0
	v_pk_mul_f32 v[158:159], v[200:201], v[158:159]
	s_nop 0
	v_pk_mul_f32 v[154:155], v[154:155], v[158:159]
	s_nop 0
	v_add_f32_e32 v161, v154, v155
	v_pk_mul_f32 v[154:155], v[156:157], v[158:159]
	s_nop 0
	v_add_f32_e32 v155, v154, v155
	v_cvt_pk_f16_f32 v154, v163, v160
	v_cvt_pk_f16_f32 v155, v161, v155
	ds_write_b64 v170, v[154:155] offset:59392
	v_pk_mul_f32 v[154:155], v[18:19], v[162:163] op_sel_hi:[1,0]
	s_nop 0
	v_pk_mul_f32 v[154:155], v[198:199], v[154:155]
	s_waitcnt vmcnt(5)
	v_pk_mul_f32 v[156:157], v[150:151], v[154:155]
	v_pk_mul_f32 v[154:155], v[152:153], v[154:155]
	v_add_f32_e32 v158, v156, v157
	v_add_f32_e32 v159, v154, v155
	v_pk_mul_f32 v[154:155], v[20:21], v[162:163] op_sel_hi:[1,0]
	s_nop 0
	v_pk_mul_f32 v[154:155], v[196:197], v[154:155]
	s_waitcnt vmcnt(4)
	v_pk_mul_f32 v[156:157], v[146:147], v[154:155]
	v_pk_mul_f32 v[154:155], v[148:149], v[154:155]
	v_add_f32_e32 v156, v156, v157
	v_add_f32_e32 v155, v154, v155
	v_cvt_pk_f16_f32 v154, v158, v159
	v_cvt_pk_f16_f32 v155, v156, v155
	ds_write_b64 v170, v[154:155] offset:59168
	v_pk_mul_f32 v[154:155], v[22:23], v[164:165] op_sel_hi:[1,0]
	s_nop 0
	v_pk_mul_f32 v[154:155], v[198:199], v[154:155]
	s_nop 0
	v_pk_mul_f32 v[150:151], v[150:151], v[154:155]
	s_nop 0
	v_add_f32_e32 v156, v150, v151
	v_pk_mul_f32 v[150:151], v[152:153], v[154:155]
	v_add_u32_e32 v154, 0xe700, v194
	v_add_f32_e32 v152, v150, v151
	v_pk_mul_f32 v[150:151], v[24:25], v[164:165] op_sel_hi:[1,0]
	v_lshlrev_b32_e32 v194, 4, v1
	v_pk_mul_f32 v[150:151], v[196:197], v[150:151]
	v_lshl_add_u64 v[166:167], s[2:3], 0, v[194:195]
	v_pk_mul_f32 v[146:147], v[146:147], v[150:151]
	s_lshl_b32 s2, s4, 11
	v_add_f32_e32 v153, v146, v147
	v_pk_mul_f32 v[146:147], v[148:149], v[150:151]
	s_or_b32 s2, s2, s25
	v_add_f32_e32 v147, v146, v147
	v_cvt_pk_f16_f32 v146, v156, v152
	v_cvt_pk_f16_f32 v147, v153, v147
	ds_write_b64 v170, v[146:147] offset:59424
	ds_read_b128 v[146:149], v232 offset:2816
	ds_read_b128 v[150:153], v232 offset:6912
	v_or_b32_e32 v168, s2, v228
	v_ashrrev_i32_e32 v169, 31, v168
	s_waitcnt lgkmcnt(1)
	v_add_f32_e32 v146, v146, v147
	v_add_f32_e32 v146, v148, v146
	v_add_f32_e32 v146, v149, v146
	v_fmamk_f32 v146, v146, 0x3c000000, v233
	v_rsq_f32_e32 v146, v146
	s_waitcnt lgkmcnt(0)
	v_add_f32_e32 v147, v150, v151
	v_add_f32_e32 v147, v152, v147
	v_add_f32_e32 v147, v153, v147
	v_pk_mul_f32 v[150:151], v[14:15], v[146:147] op_sel_hi:[1,0]
	v_fmac_f32_e32 v233, 0x3c000000, v147
	v_pk_mul_f32 v[150:151], v[212:213], v[150:151]
	v_rsq_f32_e32 v148, v233
	s_waitcnt vmcnt(3)
	v_pk_mul_f32 v[152:153], v[142:143], v[150:151]
	v_pk_mul_f32 v[150:151], v[144:145], v[150:151]
	v_add_f32_e32 v147, v152, v153
	v_add_f32_e32 v149, v150, v151
	v_pk_mul_f32 v[150:151], v[16:17], v[146:147] op_sel_hi:[1,0]
	s_nop 0
	v_pk_mul_f32 v[150:151], v[200:201], v[150:151]
	s_waitcnt vmcnt(2)
	v_pk_mul_f32 v[152:153], v[138:139], v[150:151]
	v_pk_mul_f32 v[150:151], v[140:141], v[150:151]
	v_add_f32_e32 v152, v152, v153
	v_add_f32_e32 v151, v150, v151
	v_cvt_pk_f16_f32 v150, v147, v149
	v_cvt_pk_f16_f32 v151, v152, v151
	ds_write_b64 v154, v[150:151] offset:25344
	v_pk_mul_f32 v[150:151], v[10:11], v[148:149] op_sel_hi:[1,0]
	s_nop 0
	v_pk_mul_f32 v[150:151], v[212:213], v[150:151]
	s_nop 0
	v_pk_mul_f32 v[142:143], v[142:143], v[150:151]
	s_nop 0
	v_add_f32_e32 v147, v142, v143
	v_pk_mul_f32 v[142:143], v[144:145], v[150:151]
	s_nop 0
	v_add_f32_e32 v144, v142, v143
	v_pk_mul_f32 v[142:143], v[12:13], v[148:149] op_sel_hi:[1,0]
	s_nop 0
	v_pk_mul_f32 v[142:143], v[200:201], v[142:143]
	s_nop 0
	v_pk_mul_f32 v[138:139], v[138:139], v[142:143]
	s_nop 0
	v_add_f32_e32 v145, v138, v139
	v_pk_mul_f32 v[138:139], v[140:141], v[142:143]
	s_nop 0
	v_add_f32_e32 v139, v138, v139
	v_cvt_pk_f16_f32 v138, v147, v144
	v_cvt_pk_f16_f32 v139, v145, v139
	ds_write_b64 v154, v[138:139] offset:25600
	v_pk_mul_f32 v[138:139], v[2:3], v[146:147] op_sel_hi:[1,0]
	s_nop 0
	v_pk_mul_f32 v[138:139], v[198:199], v[138:139]
	s_waitcnt vmcnt(1)
	v_pk_mul_f32 v[140:141], v[134:135], v[138:139]
	v_pk_mul_f32 v[138:139], v[136:137], v[138:139]
	v_add_f32_e32 v142, v140, v141
	v_add_f32_e32 v143, v138, v139
	v_pk_mul_f32 v[138:139], v[4:5], v[146:147] op_sel_hi:[1,0]
	s_nop 0
	v_pk_mul_f32 v[138:139], v[196:197], v[138:139]
	s_waitcnt vmcnt(0)
	v_pk_mul_f32 v[140:141], v[130:131], v[138:139]
	v_pk_mul_f32 v[138:139], v[132:133], v[138:139]
	v_add_f32_e32 v140, v140, v141
	v_add_f32_e32 v139, v138, v139
	v_cvt_pk_f16_f32 v138, v142, v143
	v_cvt_pk_f16_f32 v139, v140, v139
	ds_write_b64 v154, v[138:139] offset:25376
	v_pk_mul_f32 v[138:139], v[6:7], v[148:149] op_sel_hi:[1,0]
	s_nop 0
	v_pk_mul_f32 v[138:139], v[198:199], v[138:139]
	s_nop 0
	v_pk_mul_f32 v[134:135], v[134:135], v[138:139]
	s_nop 0
	v_add_f32_e32 v140, v134, v135
	v_pk_mul_f32 v[134:135], v[136:137], v[138:139]
	s_nop 0
	v_add_f32_e32 v136, v134, v135
	v_pk_mul_f32 v[134:135], v[8:9], v[148:149] op_sel_hi:[1,0]
	s_nop 0
	v_pk_mul_f32 v[134:135], v[196:197], v[134:135]
	s_nop 0
	v_pk_mul_f32 v[130:131], v[130:131], v[134:135]
	s_nop 0
	v_add_f32_e32 v137, v130, v131
	v_pk_mul_f32 v[130:131], v[132:133], v[134:135]
	v_lshlrev_b64 v[134:135], 8, v[168:169]
	v_add_f32_e32 v131, v130, v131
	v_cvt_pk_f16_f32 v130, v140, v136
	v_cvt_pk_f16_f32 v131, v137, v131
	ds_write_b64 v154, v[130:131] offset:25632
	v_mul_u32_u24_e32 v130, 0x210, v228
	v_add3_u32 v144, 0, v130, v194
	s_waitcnt lgkmcnt(0)
	s_barrier
	ds_read_b128 v[130:133], v144
	v_lshl_add_u64 v[138:139], v[166:167], 0, v[134:135]
	ds_read_b128 v[134:137], v144 offset:256
	v_add_u32_e32 v152, 0x8400, v144
	v_add_u32_e32 v160, 0x8400, v152
	s_waitcnt lgkmcnt(1)
	global_store_dwordx4 v[138:139], v[130:133], off sc0 sc1
	s_nop 1
	v_or_b32_e32 v130, 0x200, v0
	v_lshrrev_b32_e32 v138, 4, v130
	v_mul_u32_u24_e32 v130, 0x210, v138
	v_add3_u32 v140, 0, v130, v194
	ds_read_b128 v[130:133], v140
	v_or_b32_e32 v170, s2, v138
	v_ashrrev_i32_e32 v171, 31, v170
	v_lshlrev_b64 v[138:139], 8, v[170:171]
	v_lshl_add_u64 v[142:143], v[166:167], 0, v[138:139]
	ds_read_b128 v[138:141], v140 offset:256
	s_waitcnt lgkmcnt(1)
	global_store_dwordx4 v[142:143], v[130:133], off sc0 sc1
	ds_read_b128 v[130:133], v144 offset:33792
	v_or_b32_e32 v142, 64, v168
	v_ashrrev_i32_e32 v143, 31, v142
	v_lshlrev_b64 v[142:143], 8, v[142:143]
	v_lshl_add_u64 v[146:147], v[166:167], 0, v[142:143]
	s_waitcnt lgkmcnt(0)
	global_store_dwordx4 v[146:147], v[130:133], off sc0 sc1
	ds_read_b128 v[142:145], v144 offset:34048
	s_nop 0
	v_or_b32_e32 v130, 0x600, v0
	v_lshrrev_b32_e32 v146, 4, v130
	v_mul_u32_u24_e32 v130, 0x210, v146
	v_add3_u32 v148, 0, v130, v194
	ds_read_b128 v[130:133], v148
	v_or_b32_e32 v172, s2, v146
	v_ashrrev_i32_e32 v173, 31, v172
	v_lshlrev_b64 v[146:147], 8, v[172:173]
	v_lshl_add_u64 v[150:151], v[166:167], 0, v[146:147]
	ds_read_b128 v[146:149], v148 offset:256
	s_waitcnt lgkmcnt(1)
	global_store_dwordx4 v[150:151], v[130:133], off sc0 sc1
	ds_read_b128 v[130:133], v152 offset:33792
	v_or_b32_e32 v150, 0x80, v168
	v_ashrrev_i32_e32 v151, 31, v150
	v_lshlrev_b64 v[150:151], 8, v[150:151]
	v_lshl_add_u64 v[154:155], v[166:167], 0, v[150:151]
	s_waitcnt lgkmcnt(0)
	global_store_dwordx4 v[154:155], v[130:133], off sc0 sc1
	ds_read_b128 v[150:153], v152 offset:34048
	s_nop 0
	v_or_b32_e32 v130, 0xa00, v0
	v_lshrrev_b32_e32 v154, 4, v130
	v_mul_u32_u24_e32 v130, 0x210, v154
	v_add3_u32 v156, 0, v130, v194
	ds_read_b128 v[130:133], v156
	v_or_b32_e32 v174, s2, v154
	v_ashrrev_i32_e32 v175, 31, v174
	v_lshlrev_b64 v[154:155], 8, v[174:175]
	v_lshl_add_u64 v[158:159], v[166:167], 0, v[154:155]
	ds_read_b128 v[154:157], v156 offset:256
	s_waitcnt lgkmcnt(1)
	global_store_dwordx4 v[158:159], v[130:133], off sc0 sc1
	ds_read_b128 v[130:133], v160 offset:33792
	v_or_b32_e32 v158, 0xc0, v168
	v_ashrrev_i32_e32 v159, 31, v158
	v_lshlrev_b64 v[158:159], 8, v[158:159]
	v_lshl_add_u64 v[162:163], v[166:167], 0, v[158:159]
	s_waitcnt lgkmcnt(0)
	global_store_dwordx4 v[162:163], v[130:133], off sc0 sc1
	ds_read_b128 v[158:161], v160 offset:34048
	s_nop 0
	v_or_b32_e32 v130, 0xe00, v0
	v_lshrrev_b32_e32 v169, 4, v130
	v_mul_u32_u24_e32 v130, 0x210, v169
	v_add3_u32 v164, 0, v130, v194
	ds_read_b128 v[130:133], v164
	v_or_b32_e32 v162, s2, v169
	v_ashrrev_i32_e32 v163, 31, v162
	v_lshlrev_b64 v[162:163], 8, v[162:163]
	v_lshl_add_u64 v[176:177], v[166:167], 0, v[162:163]
	s_waitcnt lgkmcnt(0)
	global_store_dwordx4 v[176:177], v[130:133], off sc0 sc1
	ds_read_b128 v[162:165], v164 offset:256
	s_addk_i32 s2, 0x800
	v_or_b32_e32 v130, 0x800, v168
	v_ashrrev_i32_e32 v131, 31, v130
	v_lshlrev_b64 v[130:131], 8, v[130:131]
	v_lshl_add_u64 v[130:131], v[166:167], 0, v[130:131]
	global_store_dwordx4 v[130:131], v[134:137], off sc0 sc1
	v_or_b32_e32 v130, 0x800, v170
	v_ashrrev_i32_e32 v131, 31, v130
	v_lshlrev_b64 v[130:131], 8, v[130:131]
	v_lshl_add_u64 v[130:131], v[166:167], 0, v[130:131]
	global_store_dwordx4 v[130:131], v[138:141], off sc0 sc1
	v_or_b32_e32 v130, 0x840, v168
	v_ashrrev_i32_e32 v131, 31, v130
	v_lshlrev_b64 v[130:131], 8, v[130:131]
	v_lshl_add_u64 v[130:131], v[166:167], 0, v[130:131]
	global_store_dwordx4 v[130:131], v[142:145], off sc0 sc1
	v_or_b32_e32 v130, 0x800, v172
	v_ashrrev_i32_e32 v131, 31, v130
	v_lshlrev_b64 v[130:131], 8, v[130:131]
	v_lshl_add_u64 v[130:131], v[166:167], 0, v[130:131]
	global_store_dwordx4 v[130:131], v[146:149], off sc0 sc1
	v_or_b32_e32 v130, 0x880, v168
	v_ashrrev_i32_e32 v131, 31, v130
	v_lshlrev_b64 v[130:131], 8, v[130:131]
	v_lshl_add_u64 v[130:131], v[166:167], 0, v[130:131]
	global_store_dwordx4 v[130:131], v[150:153], off sc0 sc1
	v_or_b32_e32 v130, 0x800, v174
	v_ashrrev_i32_e32 v131, 31, v130
	v_lshlrev_b64 v[130:131], 8, v[130:131]
	v_lshl_add_u64 v[130:131], v[166:167], 0, v[130:131]
	global_store_dwordx4 v[130:131], v[154:157], off sc0 sc1
	v_or_b32_e32 v130, 0x8c0, v168
	v_ashrrev_i32_e32 v131, 31, v130
	v_lshlrev_b64 v[130:131], 8, v[130:131]
	v_lshl_add_u64 v[130:131], v[166:167], 0, v[130:131]
	global_store_dwordx4 v[130:131], v[158:161], off sc0 sc1
	v_or_b32_e32 v130, s2, v169
	v_ashrrev_i32_e32 v131, 31, v130
	v_lshlrev_b64 v[130:131], 8, v[130:131]
	v_lshl_add_u64 v[130:131], v[166:167], 0, v[130:131]
	s_mov_b64 s[2:3], 0
	s_waitcnt lgkmcnt(0)
	global_store_dwordx4 v[130:131], v[162:165], off sc0 sc1

_Z9gemm_projPKDF16_S0_PKfPf:
	s_ashr_i32 s3, s2, 31
	s_load_dwordx4 s[4:7], s[0:1], 0x0
	s_load_dwordx2 s[44:45], s[0:1], 0x10
	s_lshr_b32 s3, s3, 29
	s_add_i32 s10, s2, s3
	s_and_b32 s3, s10, -8
	s_sub_i32 s9, s2, s3
	s_cmp_gt_i32 s9, -1
	s_cbranch_scc0 .LBB2_2
	s_lshl_b32 s8, s9, 5
	s_ashr_i32 s2, s10, 3
	s_cbranch_execz .LBB2_3
	s_branch .LBB2_4

.LBB2_4:
	s_add_i32 s2, s8, s2
	s_ashr_i32 s3, s2, 31
	s_lshr_b32 s3, s3, 25
	s_add_i32 s3, s2, s3
	s_ashr_i32 s8, s3, 7
	s_lshl_b32 s8, s8, 3
	s_sub_i32 s9, 16, s8
	s_min_i32 s9, s9, 8
	s_abs_i32 s10, s9
	v_cvt_f32_u32_e32 v1, s10
	s_sub_i32 s12, 0, s10
	s_and_b32 s3, s3, 0xffffff80
	s_sub_i32 s2, s2, s3
	v_rcp_iflag_f32_e32 v1, v1
	s_abs_i32 s3, s2
	s_xor_b32 s11, s2, s9
	s_ashr_i32 s11, s11, 31
	v_mul_f32_e32 v1, 0x4f7ffffe, v1
	v_cvt_u32_f32_e32 v1, v1
	v_lshlrev_b32_e32 v2, 4, v0
	v_and_b32_e32 v5, 64, v0
	v_add_u32_e32 v78, 0, v2
	v_readfirstlane_b32 s13, v1
	s_mul_i32 s12, s12, s13
	s_mul_hi_u32 s12, s13, s12
	s_add_i32 s13, s13, s12
	s_mul_hi_u32 s12, s3, s13
	s_mul_i32 s13, s12, s10
	s_sub_i32 s3, s3, s13
	s_add_i32 s14, s12, 1
	s_sub_i32 s13, s3, s10
	s_cmp_ge_u32 s3, s10
	s_cselect_b32 s12, s14, s12
	s_cselect_b32 s3, s13, s3
	s_add_i32 s13, s12, 1
	s_cmp_ge_u32 s3, s10
	s_cselect_b32 s3, s13, s12
	s_xor_b32 s3, s3, s11
	s_sub_i32 s3, s3, s11
	s_lshl_b32 s10, s3, 7
	s_mul_i32 s9, s3, s9
	s_ashr_i32 s11, s10, 31
	s_sub_i32 s9, s2, s9
	v_and_b32_e32 v1, 32, v0
	s_lshl_b64 s[12:13], s[10:11], 12
	v_bitop3_b32 v4, v2, v1, 48 bitop3:0x6c
	s_waitcnt lgkmcnt(0)
	s_lshl_b64 s[46:47], s[10:11], 2
	s_add_u32 s44, s44, s46
	s_addc_u32 s45, s45, s47
	v_and_b32_e32 v179, 31, v0
	v_lshlrev_b32_e32 v179, 4, v179
	global_load_dwordx4 v[180:183], v179, s[44:45]
	s_add_u32 s2, s6, s12
	v_bfe_u32 v3, v0, 2, 4
	v_or_b32_e32 v66, v4, v5
	s_addc_u32 s3, s7, s13
	v_mov_b32_e32 v67, 0
	v_lshrrev_b32_e32 v1, 3, v0
	v_add_u32_e32 v79, 0x8000, v78
	s_add_i32 s8, s8, s9
	v_lshl_add_u64 v[8:9], s[2:3], 0, v[66:67]
	v_and_or_b32 v1, v1, 48, v3
	v_readfirstlane_b32 s2, v79
	v_or_b32_e32 v6, 0x2000, v2
	s_lshl_b32 s8, s8, 8
	v_lshlrev_b32_e32 v10, 12, v1
	v_mov_b32_e32 v11, v67
	s_mov_b32 m0, s2
	v_lshrrev_b32_e32 v1, 7, v6
	s_movk_i32 s2, 0x70
	v_add_u32_e32 v80, 0xa000, v78
	s_ashr_i32 s9, s8, 31
	v_lshl_add_u64 v[12:13], v[8:9], 0, v[10:11]
	v_and_or_b32 v1, v1, s2, v3
	v_readfirstlane_b32 s2, v80
	s_lshl_b64 s[14:15], s[8:9], 12
	global_load_lds_dwordx4 v[12:13], off
	s_mov_b32 m0, s2
	s_add_u32 s2, s4, s14
	v_lshlrev_b32_e32 v14, 12, v1
	v_mov_b32_e32 v15, v67
	s_addc_u32 s3, s5, s15
	v_lshl_add_u64 v[8:9], v[8:9], 0, v[14:15]
	v_lshl_add_u64 v[16:17], s[2:3], 0, v[66:67]
	v_readfirstlane_b32 s2, v78
	v_add_u32_e32 v81, 0x2000, v78
	global_load_lds_dwordx4 v[8:9], off
	v_lshl_add_u64 v[18:19], v[16:17], 0, v[10:11]
	s_mov_b32 m0, s2
	v_readfirstlane_b32 s2, v81
	global_load_lds_dwordx4 v[18:19], off
	s_mov_b32 m0, s2
	s_or_b32 s2, s8, 0x80
	s_ashr_i32 s3, s2, 31
	s_lshl_b64 s[2:3], s[2:3], 12
	s_add_u32 s2, s4, s2
	s_addc_u32 s3, s5, s3
	v_add_u32_e32 v82, 0x4000, v78
	v_lshl_add_u64 v[16:17], v[16:17], 0, v[14:15]
	v_lshl_add_u64 v[20:21], s[2:3], 0, v[66:67]
	v_readfirstlane_b32 s2, v82
	v_add_u32_e32 v84, 0x6000, v78
	s_add_i32 s9, 0, 0x14000
	global_load_lds_dwordx4 v[16:17], off
	v_lshl_add_u64 v[10:11], v[20:21], 0, v[10:11]
	s_mov_b32 m0, s2
	v_readfirstlane_b32 s2, v84
	v_add_u32_e32 v85, s9, v2
	global_load_lds_dwordx4 v[10:11], off
	v_lshl_add_u64 v[14:15], v[20:21], 0, v[14:15]
	s_mov_b32 m0, s2
	s_mov_b64 s[2:3], 0x80
	v_readfirstlane_b32 s16, v85
	v_add_u32_e32 v1, s9, v6
	global_load_lds_dwordx4 v[14:15], off
	v_lshl_add_u64 v[12:13], v[12:13], 0, s[2:3]
	s_mov_b32 m0, s16
	v_readfirstlane_b32 s16, v1
	v_add_u32_e32 v86, 0xc000, v78
	global_load_lds_dwordx4 v[12:13], off
	v_lshl_add_u64 v[8:9], v[8:9], 0, s[2:3]
	s_mov_b32 m0, s16
	v_readfirstlane_b32 s16, v86
	v_add_u32_e32 v87, 0xe000, v78
	global_load_lds_dwordx4 v[8:9], off
	v_lshl_add_u64 v[8:9], v[18:19], 0, s[2:3]
	s_mov_b32 m0, s16
	v_readfirstlane_b32 s16, v87
	global_load_lds_dwordx4 v[8:9], off
	s_mov_b32 m0, s16
	s_add_i32 s16, 0, 0x10000
	v_add_u32_e32 v88, s16, v2
	v_lshl_add_u64 v[8:9], v[16:17], 0, s[2:3]
	v_readfirstlane_b32 s17, v88
	global_load_lds_dwordx4 v[8:9], off
	v_lshl_add_u64 v[8:9], v[10:11], 0, s[2:3]
	s_mov_b32 m0, s17
	v_add_u32_e32 v1, s16, v6
	global_load_lds_dwordx4 v[8:9], off
	v_lshl_add_u64 v[8:9], v[14:15], 0, s[2:3]
	v_readfirstlane_b32 s2, v1
	s_mov_b32 m0, s2
	s_load_dwordx4 s[0:3], s[0:1], 0x10
	global_load_lds_dwordx4 v[8:9], off
	s_movk_i32 s16, 0xff
	v_cmp_lt_u32_e32 vcc, s16, v0
	s_and_saveexec_b64 s[16:17], vcc
	s_cbranch_execz .LBB2_6
	s_barrier

.LBB2_10:
	s_or_b64 exec, exec, s[4:5]
	v_and_b32_e32 v66, 15, v0
	v_lshl_or_b32 v66, v76, 6, v66
	v_lshl_add_u32 v67, v77, 8, 0
	v_mul_u32_u24_e32 v66, 0x210, v66
	v_add3_u32 v1, v67, v1, v66
	s_lshl_b64 s[4:5], s[10:11], 2
	s_waitcnt vmcnt(0)
	s_barrier
	ds_write_b128 v1, v[2:5]
	ds_write_b128 v1, v[6:9] offset:64
	ds_write_b128 v1, v[10:13] offset:128
	ds_write_b128 v1, v[14:17] offset:192
	ds_write_b128 v1, v[18:21] offset:8448
	ds_write_b128 v1, v[22:25] offset:8512
	ds_write_b128 v1, v[26:29] offset:8576
	ds_write_b128 v1, v[30:33] offset:8640
	ds_write_b128 v1, v[34:37] offset:16896
	ds_write_b128 v1, v[38:41] offset:16960
	ds_write_b128 v1, v[42:45] offset:17024
	ds_write_b128 v1, v[46:49] offset:17088
	ds_write_b128 v1, v[50:53] offset:25344
	ds_write_b128 v1, v[54:57] offset:25408
	ds_write_b128 v1, v[58:61] offset:25472
	ds_write_b128 v1, v[62:65] offset:25536
	v_and_b32_e32 v1, 31, v0
	s_add_u32 s0, s0, s4
	s_addc_u32 s1, s1, s5
	v_lshlrev_b32_e32 v8, 4, v1
	s_waitcnt lgkmcnt(0)
	s_barrier
	v_mov_b32_e32 v2, v180
	v_mov_b32_e32 v3, v181
	v_mov_b32_e32 v4, v182
	v_mov_b32_e32 v5, v183
	v_lshrrev_b32_e32 v1, 5, v0
	v_or_b32_e32 v7, 0x200, v0
	v_or_b32_e32 v10, 0x600, v0
	v_or_b32_e32 v6, s8, v1
	v_lshrrev_b32_e32 v11, 5, v7
	s_movk_i32 s0, 0x210
	v_lshrrev_b32_e32 v12, 5, v10
	v_add_u32_e32 v50, 0, v8
	v_ashrrev_i32_e32 v7, 31, v6
	v_or_b32_e32 v10, s8, v11
	v_or_b32_e32 v18, 32, v6
	v_or_b32_e32 v20, s8, v12
	v_mad_u32_u24 v1, v1, s0, v50
	v_lshlrev_b64 v[42:43], 13, v[6:7]
	v_mad_u32_u24 v7, v11, s0, v50
	v_ashrrev_i32_e32 v11, 31, v10
	v_ashrrev_i32_e32 v19, 31, v18
	v_mad_u32_u24 v34, v12, s0, v50
	v_ashrrev_i32_e32 v21, 31, v20
	v_lshlrev_b64 v[44:45], 13, v[10:11]
	ds_read_b128 v[10:13], v1
	ds_read_b128 v[14:17], v1 offset:16896
	v_add_u32_e32 v38, 0x8400, v1
	s_add_u32 s2, s2, s4
	v_add_u32_e32 v51, 0x4200, v1
	v_lshlrev_b64 v[46:47], 13, v[18:19]
	v_lshlrev_b64 v[48:49], 13, v[20:21]
	ds_read_b128 v[18:21], v1 offset:33792
	ds_read_b128 v[22:25], v1 offset:50688
	ds_read_b128 v[26:29], v7
	ds_read_b128 v[30:33], v51 offset:50688
	ds_read_b128 v[34:37], v34
	ds_read_b128 v[38:41], v38 offset:50688
	v_mov_b32_e32 v9, 0
	s_addc_u32 s3, s3, s5
	v_lshl_add_u64 v[8:9], s[2:3], 0, v[8:9]
	v_lshl_add_u64 v[42:43], v[8:9], 0, v[42:43]
	v_lshl_add_u64 v[44:45], v[8:9], 0, v[44:45]
	v_lshl_add_u64 v[46:47], v[8:9], 0, v[46:47]
	v_lshl_add_u64 v[48:49], v[8:9], 0, v[48:49]
	v_or_b32_e32 v7, 0xa00, v0
	v_lshrrev_b32_e32 v7, 5, v7
	v_add_u32_e32 v1, 0xc600, v1
	s_waitcnt vmcnt(0) lgkmcnt(7)
	v_pk_add_f32 v[12:13], v[4:5], v[12:13]
	v_pk_add_f32 v[10:11], v[2:3], v[10:11]
	s_waitcnt lgkmcnt(3)
	v_pk_add_f32 v[28:29], v[4:5], v[28:29]
	v_pk_add_f32 v[26:27], v[2:3], v[26:27]
	v_pk_add_f32 v[16:17], v[4:5], v[16:17]
	v_pk_add_f32 v[14:15], v[2:3], v[14:15]
	s_waitcnt lgkmcnt(1)
	v_pk_add_f32 v[36:37], v[4:5], v[36:37]
	v_pk_add_f32 v[34:35], v[2:3], v[34:35]
	global_store_dwordx4 v[42:43], v[10:13], off nt
	global_store_dwordx4 v[44:45], v[26:29], off nt
	global_store_dwordx4 v[46:47], v[14:17], off nt
	global_store_dwordx4 v[48:49], v[34:37], off nt
	v_or_b32_e32 v10, 64, v6
	v_ashrrev_i32_e32 v11, 31, v10
	v_lshlrev_b64 v[14:15], 13, v[10:11]
	v_mad_u32_u24 v10, v7, s0, v50
	ds_read_b128 v[10:13], v10
	v_pk_add_f32 v[20:21], v[4:5], v[20:21]
	v_pk_add_f32 v[18:19], v[2:3], v[18:19]
	v_lshl_add_u64 v[14:15], v[8:9], 0, v[14:15]
	global_store_dwordx4 v[14:15], v[18:21], off nt
	ds_read_b128 v[14:17], v1 offset:50688
	s_waitcnt lgkmcnt(1)
	v_pk_add_f32 v[12:13], v[4:5], v[12:13]
	v_or_b32_e32 v18, s8, v7
	v_ashrrev_i32_e32 v19, 31, v18
	v_lshlrev_b64 v[18:19], 13, v[18:19]
	v_pk_add_f32 v[10:11], v[2:3], v[10:11]
	v_lshl_add_u64 v[18:19], v[8:9], 0, v[18:19]
	v_or_b32_e32 v1, 0xe00, v0
	global_store_dwordx4 v[18:19], v[10:13], off nt
	v_or_b32_e32 v18, 0x60, v6
	v_lshrrev_b32_e32 v1, 5, v1
	v_ashrrev_i32_e32 v19, 31, v18
	v_mad_u32_u24 v7, v1, s0, v50
	v_pk_add_f32 v[10:11], v[2:3], v[22:23]
	v_lshlrev_b64 v[22:23], 13, v[18:19]
	ds_read_b128 v[18:21], v7
	v_pk_add_f32 v[12:13], v[4:5], v[24:25]
	v_lshl_add_u64 v[22:23], v[8:9], 0, v[22:23]
	global_store_dwordx4 v[22:23], v[10:13], off nt
	v_or_b32_e32 v22, s8, v1
	v_ashrrev_i32_e32 v23, 31, v22
	v_lshlrev_b64 v[22:23], 13, v[22:23]
	s_waitcnt lgkmcnt(0)
	v_pk_add_f32 v[20:21], v[4:5], v[20:21]
	v_pk_add_f32 v[18:19], v[2:3], v[18:19]
	v_lshl_add_u64 v[22:23], v[8:9], 0, v[22:23]
	global_store_dwordx4 v[22:23], v[18:21], off nt
	v_or_b32_e32 v22, 0x80, v6
	v_ashrrev_i32_e32 v23, 31, v22
	v_or_b32_e32 v1, 0x1200, v0
	v_add_u32_e32 v7, 0xc600, v51
	v_lshlrev_b64 v[22:23], 13, v[22:23]
	v_lshrrev_b32_e32 v1, 5, v1
	ds_read_b128 v[10:13], v7 offset:50688
	v_pk_add_f32 v[20:21], v[4:5], v[32:33]
	v_pk_add_f32 v[18:19], v[2:3], v[30:31]
	v_lshl_add_u64 v[22:23], v[8:9], 0, v[22:23]
	v_mad_u32_u24 v7, v1, s0, v50
	global_store_dwordx4 v[22:23], v[18:21], off nt
	ds_read_b128 v[18:21], v7
	v_or_b32_e32 v7, 0x1600, v0
	v_or_b32_e32 v26, s8, v1
	v_lshrrev_b32_e32 v7, 5, v7
	v_ashrrev_i32_e32 v27, 31, v26
	v_mad_u32_u24 v22, v7, s0, v50
	v_lshlrev_b64 v[26:27], 13, v[26:27]
	ds_read_b128 v[22:25], v22
	s_waitcnt lgkmcnt(1)
	v_pk_add_f32 v[20:21], v[4:5], v[20:21]
	v_pk_add_f32 v[18:19], v[2:3], v[18:19]
	v_lshl_add_u64 v[26:27], v[8:9], 0, v[26:27]
	global_store_dwordx4 v[26:27], v[18:21], off nt
	v_or_b32_e32 v26, 0xa0, v6
	v_ashrrev_i32_e32 v27, 31, v26
	v_lshlrev_b64 v[26:27], 13, v[26:27]
	v_pk_add_f32 v[20:21], v[4:5], v[40:41]
	v_pk_add_f32 v[18:19], v[2:3], v[38:39]
	v_lshl_add_u64 v[26:27], v[8:9], 0, v[26:27]
	global_store_dwordx4 v[26:27], v[18:21], off nt
	v_or_b32_e32 v1, 0x1a00, v0
	v_lshrrev_b32_e32 v1, 5, v1
	s_waitcnt lgkmcnt(0)
	v_pk_add_f32 v[18:19], v[2:3], v[22:23]
	v_or_b32_e32 v22, s8, v7
	v_ashrrev_i32_e32 v23, 31, v22
	v_lshlrev_b64 v[22:23], 13, v[22:23]
	v_pk_add_f32 v[20:21], v[4:5], v[24:25]
	v_lshl_add_u64 v[22:23], v[8:9], 0, v[22:23]
	global_store_dwordx4 v[22:23], v[18:21], off nt
	v_pk_add_f32 v[16:17], v[4:5], v[16:17]
	v_pk_add_f32 v[14:15], v[2:3], v[14:15]
	v_or_b32_e32 v18, 0xc0, v6
	v_ashrrev_i32_e32 v19, 31, v18
	v_lshlrev_b64 v[18:19], 13, v[18:19]
	v_lshl_add_u64 v[18:19], v[8:9], 0, v[18:19]
	v_mad_u32_u24 v7, v1, s0, v50
	v_or_b32_e32 v0, 0x1e00, v0
	global_store_dwordx4 v[18:19], v[14:17], off nt
	ds_read_b128 v[14:17], v7
	v_lshrrev_b32_e32 v7, 5, v0
	v_mad_u32_u24 v0, v7, s0, v50
	ds_read_b128 v[18:21], v0
	v_or_b32_e32 v0, s8, v1
	v_ashrrev_i32_e32 v1, 31, v0
	v_lshlrev_b64 v[0:1], 13, v[0:1]
	s_waitcnt lgkmcnt(1)
	v_pk_add_f32 v[16:17], v[4:5], v[16:17]
	v_pk_add_f32 v[14:15], v[2:3], v[14:15]
	v_lshl_add_u64 v[0:1], v[8:9], 0, v[0:1]
	global_store_dwordx4 v[0:1], v[14:17], off nt
	v_or_b32_e32 v0, 0xe0, v6
	v_ashrrev_i32_e32 v1, 31, v0
	v_lshlrev_b64 v[0:1], 13, v[0:1]
	v_pk_add_f32 v[12:13], v[4:5], v[12:13]
	v_pk_add_f32 v[10:11], v[2:3], v[10:11]
	v_lshl_add_u64 v[0:1], v[8:9], 0, v[0:1]
	global_store_dwordx4 v[0:1], v[10:13], off nt
	v_add_u32_e32 v0, s8, v7
	v_ashrrev_i32_e32 v1, 31, v0
	v_lshlrev_b64 v[0:1], 13, v[0:1]
	s_waitcnt lgkmcnt(0)
	v_pk_add_f32 v[4:5], v[4:5], v[20:21]
	v_pk_add_f32 v[2:3], v[2:3], v[18:19]
	v_lshl_add_u64 v[0:1], v[8:9], 0, v[0:1]
	global_store_dwordx4 v[0:1], v[2:5], off nt
	s_endpgm

	.amdhsa_kernel _Z9gemm_projPKDF16_S0_PKfPf
		.amdhsa_group_segment_fixed_size 0
		.amdhsa_private_segment_fixed_size 0
		.amdhsa_kernarg_size 32
		.amdhsa_user_sgpr_count 2
		.amdhsa_user_sgpr_dispatch_ptr 0
		.amdhsa_user_sgpr_queue_ptr 0
		.amdhsa_user_sgpr_kernarg_segment_ptr 1
		.amdhsa_user_sgpr_dispatch_id 0
		.amdhsa_user_sgpr_kernarg_preload_length 0
		.amdhsa_user_sgpr_kernarg_preload_offset 0
		.amdhsa_user_sgpr_private_segment_size 0
		.amdhsa_uses_dynamic_stack 0
		.amdhsa_enable_private_segment 0
		.amdhsa_system_sgpr_workgroup_id_x 1
		.amdhsa_system_sgpr_workgroup_id_y 0
		.amdhsa_system_sgpr_workgroup_id_z 0
		.amdhsa_system_sgpr_workgroup_info 0
		.amdhsa_system_vgpr_workitem_id 0
		.amdhsa_next_free_vgpr 184
		.amdhsa_next_free_sgpr 48
		.amdhsa_accum_offset 184
		.amdhsa_reserve_vcc 1
		.amdhsa_float_round_mode_32 0
		.amdhsa_float_round_mode_16_64 0
		.amdhsa_float_denorm_mode_32 3
		.amdhsa_float_denorm_mode_16_64 3
		.amdhsa_dx10_clamp 1
		.amdhsa_ieee_mode 1
		.amdhsa_fp16_overflow 0
		.amdhsa_tg_split 0
		.amdhsa_exception_fp_ieee_invalid_op 0
		.amdhsa_exception_fp_denorm_src 0
		.amdhsa_exception_fp_ieee_div_zero 0
		.amdhsa_exception_fp_ieee_overflow 0
		.amdhsa_exception_fp_ieee_underflow 0
		.amdhsa_exception_fp_ieee_inexact 0
		.amdhsa_exception_int_div_zero 0
	.end_amdhsa_kernel

amdhsa.kernels:
  - .agpr_count:     0
    .args:
      - .actual_access:  read_only
        .address_space:  global
        .offset:         0
        .size:           8
        .value_kind:     global_buffer
      - .actual_access:  write_only
        .address_space:  global
        .offset:         8
        .size:           8
        .value_kind:     global_buffer
      - .offset:         16
        .size:           8
        .value_kind:     by_value
      - .actual_access:  read_only
        .address_space:  global
        .offset:         24
        .size:           8
        .value_kind:     global_buffer
      - .actual_access:  write_only
        .address_space:  global
        .offset:         32
        .size:           8
        .value_kind:     global_buffer
      - .offset:         40
        .size:           8
        .value_kind:     by_value
      - .actual_access:  read_only
        .address_space:  global
        .offset:         48
        .size:           8
        .value_kind:     global_buffer
      - .actual_access:  write_only
        .address_space:  global
        .offset:         56
        .size:           8
        .value_kind:     global_buffer
      - .offset:         64
        .size:           8
        .value_kind:     by_value
      - .offset:         72
        .size:           4
        .value_kind:     hidden_block_count_x
      - .offset:         76
        .size:           4
        .value_kind:     hidden_block_count_y
      - .offset:         80
        .size:           4
        .value_kind:     hidden_block_count_z
      - .offset:         84
        .size:           2
        .value_kind:     hidden_group_size_x
      - .offset:         86
        .size:           2
        .value_kind:     hidden_group_size_y
      - .offset:         88
        .size:           2
        .value_kind:     hidden_group_size_z
      - .offset:         90
        .size:           2
        .value_kind:     hidden_remainder_x
      - .offset:         92
        .size:           2
        .value_kind:     hidden_remainder_y
      - .offset:         94
        .size:           2
        .value_kind:     hidden_remainder_z
      - .offset:         112
        .size:           8
        .value_kind:     hidden_global_offset_x
      - .offset:         120
        .size:           8
        .value_kind:     hidden_global_offset_y
      - .offset:         128
        .size:           8
        .value_kind:     hidden_global_offset_z
      - .offset:         136
        .size:           2
        .value_kind:     hidden_grid_dims
    .group_segment_fixed_size: 0
    .kernarg_segment_align: 8
    .kernarg_segment_size: 328
    .language:       OpenCL C
    .language_version:
      - 2
      - 0
    .max_flat_workgroup_size: 256
    .name:           _Z12cvt3_f32_f16PKfPDF16_lS0_S1_lS0_S1_l
    .private_segment_fixed_size: 0
    .sgpr_count:     34
    .sgpr_spill_count: 0
    .symbol:         _Z12cvt3_f32_f16PKfPDF16_lS0_S1_lS0_S1_l.kd
    .uniform_work_group_size: 1
    .uses_dynamic_stack: false
    .vgpr_count:     16
    .vgpr_spill_count: 0
    .wavefront_size: 64
  - .agpr_count:     0
    .args:
      - .address_space:  global
        .offset:         0
        .size:           8
        .value_kind:     global_buffer
      - .address_space:  global
        .offset:         8
        .size:           8
        .value_kind:     global_buffer
      - .actual_access:  read_only
        .address_space:  global
        .offset:         16
        .size:           8
        .value_kind:     global_buffer
      - .actual_access:  read_only
        .address_space:  global
        .offset:         24
        .size:           8
        .value_kind:     global_buffer
      - .actual_access:  read_only
        .address_space:  global
        .offset:         32
        .size:           8
        .value_kind:     global_buffer
      - .actual_access:  write_only
        .address_space:  global
        .offset:         40
        .size:           8
        .value_kind:     global_buffer
      - .actual_access:  write_only
        .address_space:  global
        .offset:         48
        .size:           8
        .value_kind:     global_buffer
      - .actual_access:  write_only
        .address_space:  global
        .offset:         56
        .size:           8
        .value_kind:     global_buffer
    .group_segment_fixed_size: 0
    .kernarg_segment_align: 8
    .kernarg_segment_size: 64
    .language:       OpenCL C
    .language_version:
      - 2
      - 0
    .max_flat_workgroup_size: 512
    .name:           _Z8gemm_qkvPKDF16_S0_PKfS2_S2_PDF16_S3_S3_
    .private_segment_fixed_size: 0
    .sgpr_count:     73
    .sgpr_spill_count: 0
    .symbol:         _Z8gemm_qkvPKDF16_S0_PKfS2_S2_PDF16_S3_S3_.kd
    .uniform_work_group_size: 1
    .uses_dynamic_stack: false
    .vgpr_count:     256
    .vgpr_spill_count: 0
    .wavefront_size: 64
  - .agpr_count:     0
    .args:
      - .address_space:  global
        .offset:         0
        .size:           8
        .value_kind:     global_buffer
      - .address_space:  global
        .offset:         8
        .size:           8
        .value_kind:     global_buffer
      - .actual_access:  read_only
        .address_space:  global
        .offset:         16
        .size:           8
        .value_kind:     global_buffer
      - .actual_access:  write_only
        .address_space:  global
        .offset:         24
        .size:           8
        .value_kind:     global_buffer
    .group_segment_fixed_size: 0
    .kernarg_segment_align: 8
    .kernarg_segment_size: 32
    .language:       OpenCL C
    .language_version:
      - 2
      - 0
    .max_flat_workgroup_size: 512
    .name:           _Z9gemm_projPKDF16_S0_PKfPf
    .private_segment_fixed_size: 0
    .sgpr_count:     54
    .sgpr_spill_count: 0
    .symbol:         _Z9gemm_projPKDF16_S0_PKfPf.kd
    .uniform_work_group_size: 1
    .uses_dynamic_stack: false
    .vgpr_count:     184
    .vgpr_spill_count: 0
    .wavefront_size: 64
  - .agpr_count:     256
    .args:
      - .address_space:  global
        .offset:         0
        .size:           8
        .value_kind:     global_buffer
      - .address_space:  global
        .offset:         8
        .size:           8
        .value_kind:     global_buffer
      - .address_space:  global
        .offset:         16
        .size:           8
        .value_kind:     global_buffer
      - .actual_access:  write_only
        .address_space:  global
        .offset:         24
        .size:           8
        .value_kind:     global_buffer
      - .offset:         32
        .size:           4
        .value_kind:     hidden_block_count_x
      - .offset:         36
        .size:           4
        .value_kind:     hidden_block_count_y
      - .offset:         40
        .size:           4
        .value_kind:     hidden_block_count_z
      - .offset:         44
        .size:           2
        .value_kind:     hidden_group_size_x
      - .offset:         46
        .size:           2
        .value_kind:     hidden_group_size_y
      - .offset:         48
        .size:           2
        .value_kind:     hidden_group_size_z
      - .offset:         50
        .size:           2
        .value_kind:     hidden_remainder_x
      - .offset:         52
        .size:           2
        .value_kind:     hidden_remainder_y
      - .offset:         54
        .size:           2
        .value_kind:     hidden_remainder_z
      - .offset:         72
        .size:           8
        .value_kind:     hidden_global_offset_x
      - .offset:         80
        .size:           8
        .value_kind:     hidden_global_offset_y
      - .offset:         88
        .size:           8
        .value_kind:     hidden_global_offset_z
      - .offset:         96
        .size:           2
        .value_kind:     hidden_grid_dims
      - .offset:         152
        .size:           4
        .value_kind:     hidden_dynamic_lds_size
    .group_segment_fixed_size: 0
    .kernarg_segment_align: 8
    .kernarg_segment_size: 288
    .language:       OpenCL C
    .language_version:
      - 2
      - 0
    .max_flat_workgroup_size: 256
    .name:           attn_fwd_pwg4x64
    .private_segment_fixed_size: 0
    .sgpr_count:     106
    .sgpr_spill_count: 0
    .symbol:         attn_fwd_pwg4x64.kd
    .uniform_work_group_size: 1
    .uses_dynamic_stack: false
    .vgpr_count:     508
    .vgpr_spill_count: 0
    .wavefront_size: 64
